# v64 + in the hand-written G1/G3/G5 epilogues the wr0 wave group runs at s_setprio 2 (finishes its epilogue first and starts the next unit's load phase under the other group's epilogue)
# baseline (speedup 1.0000x reference)
; __device__ __forceinline__ unsigned cvt_pk_bf16(float lo, float hi) { const f32x2c_t v = {lo, hi}; return __builtin_bit_cast(unsigned, __builtin_convertvector(v, bf16x2c_t)); }
; __device__ __forceinline__ void rstd8(const float* SS, int rowb, int lane, float (&rs)[2][4]) {
;     f32x4 p[2][4];
; #pragma unroll
;     for (int ai = 0; ai < 2; ++ai)
; #pragma unroll
;         for (int m = 0; m < 4; ++m) p[ai][m] = *(const f32x4*)(SS + (size_t)(rowb + HALF * ai + 16 * m + (lane >> 2)) * 16 + 4 * (lane & 3));
;     asm volatile("" : "+v"(p[0][0]), "+v"(p[0][1]), "+v"(p[0][2]), "+v"(p[0][3]), "+v"(p[1][0]), "+v"(p[1][1]), "+v"(p[1][2]), "+v"(p[1][3]));
; #pragma unroll
;     for (int ai = 0; ai < 2; ++ai)
; #pragma unroll
;         for (int m = 0; m < 4; ++m) { float s = (p[ai][m][0] + p[ai][m][1]) + (p[ai][m][2] + p[ai][m][3]); s += __shfl_xor(s, 1); s += __shfl_xor(s, 2);
;             const float r = __builtin_amdgcn_rsqf(s * (1.0f / 1024.0f) + RMS_EPS);
;             rs[ai][m] = __builtin_bit_cast(float, __builtin_amdgcn_ds_bpermute((lane & 15) << 4, __builtin_bit_cast(int, r))); }
; }
;     __device__ __forceinline__ void operator()(const f32x4 (&acc)[2][2][4][2], const Unit& u, int wr, int wc, int fr, int fq) const {
;         const int row0 = u.pm * BM + wr * 64 + fr, col0 = u.pn * BM + wc * 32 + 8 * fq;
;         const float sc = (u.pn == 0) ? qs : ((u.pn == 3) ? 0.125f : 1.0f);
;         const int lane = fr + 16 * fq, qs4 = QSRC_ST(lane); const int rowS = u.pm * BM + wr * 64 + (lane >> 2), colS = u.pn * BM + wc * 32 + 8 * (lane & 3);
;         float rs8[2][4]; rstd8(SS, u.pm * BM + wr * 64, lane, rs8);
; #pragma unroll
;         for (int ai = 0; ai < 2; ++ai) {
; #pragma unroll
;             for (int m = 0; m < 4; ++m) { const float rs = rs8[ai][m] * sc;
;                 bf16_t* rowp = U + (size_t)(rowS + ai * HALF + m * 16) * ldu + colS;
; #pragma unroll
;                 for (int bj = 0; bj < 2; ++bj) { const f32x4 v0 = acc[ai][bj][m][0] * rs, v1 = acc[ai][bj][m][1] * rs;
;                     u32x4 w; w.x = cvt_pk_bf16(v0[0], v0[1]); w.y = cvt_pk_bf16(v0[2], v0[3]); w.z = cvt_pk_bf16(v1[0], v1[1]); w.w = cvt_pk_bf16(v1[2], v1[3]);
;                     *(u32x4*)(rowp + bj * HALF) = lane_perm(w, qs4); } } }
.LBB0_256:
	s_and_b64 vcc, exec, s[12:13]
	s_cbranch_vccz .Lepi_prio0
	s_setprio 2
.Lepi_prio0:
	s_cmp_eq_u32 s49, 3
	s_cselect_b64 vcc, -1, 0
	v_cndmask_b32_e32 v156, 1.0, v174, vcc
	s_cmp_lg_u32 s49, 0
	s_cselect_b64 vcc, -1, 0
	v_cndmask_b32_e32 v156, v175, v156, vcc
	v_lshl_or_b32 v208, s49, 8, v169
	v_ashrrev_i32_e32 v209, 31, v208
	v_mov_b64_e32 v[154:155], s[44:45]
	v_lshlrev_b64 v[208:209], 1, v[208:209]
	v_mad_i64_i32 v[152:153], s[24:25], v164, s48, v[154:155]
	s_nop 0
	v_lshl_add_u64 v[208:209], v[152:153], 0, v[208:209]
	s_waitcnt vmcnt(0)
	v_add_f32_e32 v176, v176, v177
	v_add_f32_e32 v180, v180, v181
	v_add_f32_e32 v184, v184, v185
	v_add_f32_e32 v188, v188, v189
	v_add_f32_e32 v192, v192, v193
	v_add_f32_e32 v196, v196, v197
	v_add_f32_e32 v200, v200, v201
	v_add_f32_e32 v204, v204, v205
	v_add_f32_e32 v178, v178, v179
	v_add_f32_e32 v182, v182, v183
	v_add_f32_e32 v186, v186, v187
	v_add_f32_e32 v190, v190, v191
	v_add_f32_e32 v194, v194, v195
	v_add_f32_e32 v198, v198, v199
	v_add_f32_e32 v202, v202, v203
	v_add_f32_e32 v206, v206, v207
	v_add_f32_e32 v176, v176, v178
	v_add_f32_e32 v180, v180, v182
	v_add_f32_e32 v184, v184, v186
	v_add_f32_e32 v188, v188, v190
	v_add_f32_e32 v192, v192, v194
	v_add_f32_e32 v196, v196, v198
	v_add_f32_e32 v200, v200, v202
	v_add_f32_e32 v204, v204, v206
	v_add_f32_dpp v176, v176, v176 quad_perm:[1,0,3,2] row_mask:0xf bank_mask:0xf
	v_add_f32_dpp v180, v180, v180 quad_perm:[1,0,3,2] row_mask:0xf bank_mask:0xf
	v_add_f32_dpp v184, v184, v184 quad_perm:[1,0,3,2] row_mask:0xf bank_mask:0xf
	v_add_f32_dpp v188, v188, v188 quad_perm:[1,0,3,2] row_mask:0xf bank_mask:0xf
	v_add_f32_dpp v192, v192, v192 quad_perm:[1,0,3,2] row_mask:0xf bank_mask:0xf
	v_add_f32_dpp v196, v196, v196 quad_perm:[1,0,3,2] row_mask:0xf bank_mask:0xf
	v_add_f32_dpp v200, v200, v200 quad_perm:[1,0,3,2] row_mask:0xf bank_mask:0xf
	v_add_f32_dpp v204, v204, v204 quad_perm:[1,0,3,2] row_mask:0xf bank_mask:0xf
	v_add_f32_dpp v176, v176, v176 quad_perm:[2,3,0,1] row_mask:0xf bank_mask:0xf
	v_add_f32_dpp v180, v180, v180 quad_perm:[2,3,0,1] row_mask:0xf bank_mask:0xf
	v_add_f32_dpp v184, v184, v184 quad_perm:[2,3,0,1] row_mask:0xf bank_mask:0xf
	v_add_f32_dpp v188, v188, v188 quad_perm:[2,3,0,1] row_mask:0xf bank_mask:0xf
	v_add_f32_dpp v192, v192, v192 quad_perm:[2,3,0,1] row_mask:0xf bank_mask:0xf
	v_add_f32_dpp v196, v196, v196 quad_perm:[2,3,0,1] row_mask:0xf bank_mask:0xf
	v_add_f32_dpp v200, v200, v200 quad_perm:[2,3,0,1] row_mask:0xf bank_mask:0xf
	v_add_f32_dpp v204, v204, v204 quad_perm:[2,3,0,1] row_mask:0xf bank_mask:0xf
	v_fmamk_f32 v176, v176, 0x3a800000, v173
	v_fmamk_f32 v180, v180, 0x3a800000, v173
	v_fmamk_f32 v184, v184, 0x3a800000, v173
	v_fmamk_f32 v188, v188, 0x3a800000, v173
	v_fmamk_f32 v192, v192, 0x3a800000, v173
	v_fmamk_f32 v196, v196, 0x3a800000, v173
	v_fmamk_f32 v200, v200, 0x3a800000, v173
	v_fmamk_f32 v204, v204, 0x3a800000, v173
	ds_bpermute_b32 v176, v168, v176
	ds_bpermute_b32 v180, v168, v180
	ds_bpermute_b32 v184, v168, v184
	ds_bpermute_b32 v188, v168, v188
	ds_bpermute_b32 v192, v168, v192
	ds_bpermute_b32 v196, v168, v196
	ds_bpermute_b32 v200, v168, v200
	ds_bpermute_b32 v204, v168, v204
	s_waitcnt lgkmcnt(0)
	v_rsq_f32_e32 v178, v176
	v_rsq_f32_e32 v182, v180
	v_rsq_f32_e32 v186, v184
	v_rsq_f32_e32 v190, v188
	v_rsq_f32_e32 v194, v192
	v_rsq_f32_e32 v198, v196
	v_rsq_f32_e32 v202, v200
	v_rsq_f32_e32 v206, v204
	v_mul_f32_e32 v178, v156, v178
	v_mul_f32_e32 v182, v156, v182
	v_mul_f32_e32 v186, v156, v186
	v_mul_f32_e32 v190, v156, v190
	v_mul_f32_e32 v194, v156, v194
	v_mul_f32_e32 v198, v156, v198
	v_mul_f32_e32 v202, v156, v202
	v_mul_f32_e32 v206, v156, v206
	v_pk_mul_f32 v[126:127], v[126:127], v[178:179] op_sel_hi:[1,0]
	v_pk_mul_f32 v[128:129], v[128:129], v[178:179] op_sel_hi:[1,0]
	v_pk_mul_f32 v[122:123], v[122:123], v[178:179] op_sel_hi:[1,0]
	v_pk_mul_f32 v[124:125], v[124:125], v[178:179] op_sel_hi:[1,0]
	v_pk_mul_f32 v[118:119], v[118:119], v[178:179] op_sel_hi:[1,0]
	v_pk_mul_f32 v[120:121], v[120:121], v[178:179] op_sel_hi:[1,0]
	v_pk_mul_f32 v[110:111], v[110:111], v[178:179] op_sel_hi:[1,0]
	v_pk_mul_f32 v[112:113], v[112:113], v[178:179] op_sel_hi:[1,0]
	v_cvt_pk_bf16_f32 v126, v126, v127
	v_cvt_pk_bf16_f32 v127, v128, v129
	v_cvt_pk_bf16_f32 v128, v122, v123
	v_cvt_pk_bf16_f32 v129, v124, v125
	v_cvt_pk_bf16_f32 v118, v118, v119
	v_cvt_pk_bf16_f32 v119, v120, v121
	v_cvt_pk_bf16_f32 v120, v110, v111
	v_cvt_pk_bf16_f32 v121, v112, v113
	ds_bpermute_b32 v122, v166, v126
	ds_bpermute_b32 v123, v166, v127
	ds_bpermute_b32 v124, v166, v128
	ds_bpermute_b32 v125, v166, v129
	ds_bpermute_b32 v110, v166, v118
	ds_bpermute_b32 v111, v166, v119
	ds_bpermute_b32 v112, v166, v120
	ds_bpermute_b32 v113, v166, v121
	v_mov_b32_e32 v210, v208
	v_mov_b32_e32 v211, v209
	v_pk_mul_f32 v[114:115], v[114:115], v[182:183] op_sel_hi:[1,0]
	v_pk_mul_f32 v[116:117], v[116:117], v[182:183] op_sel_hi:[1,0]
	v_pk_mul_f32 v[106:107], v[106:107], v[182:183] op_sel_hi:[1,0]
	v_pk_mul_f32 v[108:109], v[108:109], v[182:183] op_sel_hi:[1,0]
	v_pk_mul_f32 v[102:103], v[102:103], v[182:183] op_sel_hi:[1,0]
	v_pk_mul_f32 v[104:105], v[104:105], v[182:183] op_sel_hi:[1,0]
	v_pk_mul_f32 v[94:95], v[94:95], v[182:183] op_sel_hi:[1,0]
	v_pk_mul_f32 v[96:97], v[96:97], v[182:183] op_sel_hi:[1,0]
	v_cvt_pk_bf16_f32 v114, v114, v115
	v_cvt_pk_bf16_f32 v115, v116, v117
	v_cvt_pk_bf16_f32 v116, v106, v107
	v_cvt_pk_bf16_f32 v117, v108, v109
	v_cvt_pk_bf16_f32 v102, v102, v103
	v_cvt_pk_bf16_f32 v103, v104, v105
	v_cvt_pk_bf16_f32 v104, v94, v95
	v_cvt_pk_bf16_f32 v105, v96, v97
	ds_bpermute_b32 v106, v166, v114
	ds_bpermute_b32 v107, v166, v115
	ds_bpermute_b32 v108, v166, v116
	ds_bpermute_b32 v109, v166, v117
	ds_bpermute_b32 v94, v166, v102
	ds_bpermute_b32 v95, v166, v103
	ds_bpermute_b32 v96, v166, v104
	ds_bpermute_b32 v97, v166, v105
	v_add_co_u32_e32 v212, vcc, 0x18000, v208
	v_addc_co_u32_e32 v213, vcc, 0, v209, vcc
	s_waitcnt lgkmcnt(8)
; __device__ __forceinline__ unsigned cvt_pk_bf16(float lo, float hi) { const f32x2c_t v = {lo, hi}; return __builtin_bit_cast(unsigned, __builtin_convertvector(v, bf16x2c_t)); }
;     __device__ __forceinline__ void operator()(const f32x4 (&acc)[2][2][4][2], const Unit& u, int wr, int wc, int fr, int fq) const {
;     ...
;             for (int m = 0; m < 4; ++m) { const float rs = rs8[ai][m] * sc;
;                 bf16_t* rowp = U + (size_t)(rowS + ai * HALF + m * 16) * ldu + colS;
; #pragma unroll
;                 for (int bj = 0; bj < 2; ++bj) { const f32x4 v0 = acc[ai][bj][m][0] * rs, v1 = acc[ai][bj][m][1] * rs;
;                     u32x4 w; w.x = cvt_pk_bf16(v0[0], v0[1]); w.y = cvt_pk_bf16(v0[2], v0[3]); w.z = cvt_pk_bf16(v1[0], v1[1]); w.w = cvt_pk_bf16(v1[2], v1[3]);
;                     *(u32x4*)(rowp + bj * HALF) = lane_perm(w, qs4); } } }
	global_store_dwordx4 v[210:211], v[122:125], off
	global_store_dwordx4 v[210:211], v[110:113], off offset:256
	v_pk_mul_f32 v[98:99], v[98:99], v[186:187] op_sel_hi:[1,0]
	v_pk_mul_f32 v[100:101], v[100:101], v[186:187] op_sel_hi:[1,0]
	v_pk_mul_f32 v[90:91], v[90:91], v[186:187] op_sel_hi:[1,0]
	v_pk_mul_f32 v[92:93], v[92:93], v[186:187] op_sel_hi:[1,0]
	v_pk_mul_f32 v[86:87], v[86:87], v[186:187] op_sel_hi:[1,0]
	v_pk_mul_f32 v[88:89], v[88:89], v[186:187] op_sel_hi:[1,0]
	v_pk_mul_f32 v[78:79], v[78:79], v[186:187] op_sel_hi:[1,0]
	v_pk_mul_f32 v[80:81], v[80:81], v[186:187] op_sel_hi:[1,0]
	v_cvt_pk_bf16_f32 v98, v98, v99
	v_cvt_pk_bf16_f32 v99, v100, v101
	v_cvt_pk_bf16_f32 v100, v90, v91
	v_cvt_pk_bf16_f32 v101, v92, v93
	v_cvt_pk_bf16_f32 v86, v86, v87
	v_cvt_pk_bf16_f32 v87, v88, v89
	v_cvt_pk_bf16_f32 v88, v78, v79
	v_cvt_pk_bf16_f32 v89, v80, v81
	ds_bpermute_b32 v90, v166, v98
	ds_bpermute_b32 v91, v166, v99
	ds_bpermute_b32 v92, v166, v100
	ds_bpermute_b32 v93, v166, v101
	ds_bpermute_b32 v78, v166, v86
	ds_bpermute_b32 v79, v166, v87
	ds_bpermute_b32 v80, v166, v88
	ds_bpermute_b32 v81, v166, v89
	v_add_co_u32_e32 v210, vcc, 0x30000, v208
	v_addc_co_u32_e32 v211, vcc, 0, v209, vcc
	s_waitcnt lgkmcnt(8)
	global_store_dwordx4 v[212:213], v[106:109], off
	global_store_dwordx4 v[212:213], v[94:97], off offset:256
	v_pk_mul_f32 v[82:83], v[82:83], v[190:191] op_sel_hi:[1,0]
	v_pk_mul_f32 v[84:85], v[84:85], v[190:191] op_sel_hi:[1,0]
	v_pk_mul_f32 v[74:75], v[74:75], v[190:191] op_sel_hi:[1,0]
	v_pk_mul_f32 v[76:77], v[76:77], v[190:191] op_sel_hi:[1,0]
	v_pk_mul_f32 v[70:71], v[70:71], v[190:191] op_sel_hi:[1,0]
	v_pk_mul_f32 v[72:73], v[72:73], v[190:191] op_sel_hi:[1,0]
	v_pk_mul_f32 v[66:67], v[66:67], v[190:191] op_sel_hi:[1,0]
	v_pk_mul_f32 v[68:69], v[68:69], v[190:191] op_sel_hi:[1,0]
	v_cvt_pk_bf16_f32 v82, v82, v83
	v_cvt_pk_bf16_f32 v83, v84, v85
	v_cvt_pk_bf16_f32 v84, v74, v75
	v_cvt_pk_bf16_f32 v85, v76, v77
	v_cvt_pk_bf16_f32 v70, v70, v71
	v_cvt_pk_bf16_f32 v71, v72, v73
	v_cvt_pk_bf16_f32 v72, v66, v67
	v_cvt_pk_bf16_f32 v73, v68, v69
	ds_bpermute_b32 v74, v166, v82
	ds_bpermute_b32 v75, v166, v83
	ds_bpermute_b32 v76, v166, v84
	ds_bpermute_b32 v77, v166, v85
	ds_bpermute_b32 v66, v166, v70
	ds_bpermute_b32 v67, v166, v71
	ds_bpermute_b32 v68, v166, v72
	ds_bpermute_b32 v69, v166, v73
	v_add_co_u32_e32 v212, vcc, 0x48000, v208
	v_addc_co_u32_e32 v213, vcc, 0, v209, vcc
	s_waitcnt lgkmcnt(8)
	global_store_dwordx4 v[210:211], v[90:93], off
	global_store_dwordx4 v[210:211], v[78:81], off offset:256
	v_pk_mul_f32 v[62:63], v[62:63], v[194:195] op_sel_hi:[1,0]
	v_pk_mul_f32 v[64:65], v[64:65], v[194:195] op_sel_hi:[1,0]
	v_pk_mul_f32 v[58:59], v[58:59], v[194:195] op_sel_hi:[1,0]
	v_pk_mul_f32 v[60:61], v[60:61], v[194:195] op_sel_hi:[1,0]
	v_pk_mul_f32 v[54:55], v[54:55], v[194:195] op_sel_hi:[1,0]
	v_pk_mul_f32 v[56:57], v[56:57], v[194:195] op_sel_hi:[1,0]
	v_pk_mul_f32 v[46:47], v[46:47], v[194:195] op_sel_hi:[1,0]
	v_pk_mul_f32 v[48:49], v[48:49], v[194:195] op_sel_hi:[1,0]
	v_cvt_pk_bf16_f32 v62, v62, v63
	v_cvt_pk_bf16_f32 v63, v64, v65
	v_cvt_pk_bf16_f32 v64, v58, v59
	v_cvt_pk_bf16_f32 v65, v60, v61
	v_cvt_pk_bf16_f32 v54, v54, v55
	v_cvt_pk_bf16_f32 v55, v56, v57
	v_cvt_pk_bf16_f32 v56, v46, v47
	v_cvt_pk_bf16_f32 v57, v48, v49
	ds_bpermute_b32 v58, v166, v62
	ds_bpermute_b32 v59, v166, v63
	ds_bpermute_b32 v60, v166, v64
	ds_bpermute_b32 v61, v166, v65
	ds_bpermute_b32 v46, v166, v54
	ds_bpermute_b32 v47, v166, v55
	ds_bpermute_b32 v48, v166, v56
	ds_bpermute_b32 v49, v166, v57
	v_add_co_u32_e32 v210, vcc, 0xc0000, v208
	v_addc_co_u32_e32 v211, vcc, 0, v209, vcc
	s_waitcnt lgkmcnt(8)
; __device__ __forceinline__ unsigned cvt_pk_bf16(float lo, float hi) { const f32x2c_t v = {lo, hi}; return __builtin_bit_cast(unsigned, __builtin_convertvector(v, bf16x2c_t)); }
; #define PG8_BAR __builtin_amdgcn_s_barrier()
;     __device__ __forceinline__ void operator()(const f32x4 (&acc)[2][2][4][2], const Unit& u, int wr, int wc, int fr, int fq) const {
;     ...
;             for (int m = 0; m < 4; ++m) { const float rs = rs8[ai][m] * sc;
;                 bf16_t* rowp = U + (size_t)(rowS + ai * HALF + m * 16) * ldu + colS;
; #pragma unroll
;                 for (int bj = 0; bj < 2; ++bj) { const f32x4 v0 = acc[ai][bj][m][0] * rs, v1 = acc[ai][bj][m][1] * rs;
;                     u32x4 w; w.x = cvt_pk_bf16(v0[0], v0[1]); w.y = cvt_pk_bf16(v0[2], v0[3]); w.z = cvt_pk_bf16(v1[0], v1[1]); w.w = cvt_pk_bf16(v1[2], v1[3]);
;                     *(u32x4*)(rowp + bj * HALF) = lane_perm(w, qs4); } } }
; template <class Epi, class Sched, bool ALIGN_EPI = false, bool SP2 = false>
; __device__ __forceinline__ void gemm_phase(PG8_LAS unsigned char* lds, const Gemm g, const Sched& S, const Epi& E, const bool skip_epi = false) {
;     ...
;         if constexpr (!Epi::AFTER_DRAIN) { if (!skip_epi) E(acc, cur, wr, wc, fr, fq); S.done(cur); }
;         if (!has_next) break;
; #pragma unroll
;         for (int a = 0; a < 2; ++a)
; #pragma unroll
;             for (int b = 0; b < 2; ++b)
; #pragma unroll
;                 for (int m = 0; m < 4; ++m)
; #pragma unroll
;                     for (int n = 0; n < 2; ++n) acc[a][b][m][n] = (f32x4){0.f, 0.f, 0.f, 0.f};
;         cur = nxt; cA = nA; cB = nB; ++ui;
;         if constexpr (Sched::GATHER) { gA[0][0] = gN[0][0]; gA[0][1] = gN[0][1]; gA[1][0] = gN[1][0]; gA[1][1] = gN[1][1]; }
;         if constexpr (ALIGN_EPI) { if (wr == 1) PG8_BAR; }
	global_store_dwordx4 v[212:213], v[74:77], off
	global_store_dwordx4 v[212:213], v[66:69], off offset:256
	v_pk_mul_f32 v[50:51], v[50:51], v[198:199] op_sel_hi:[1,0]
	v_pk_mul_f32 v[52:53], v[52:53], v[198:199] op_sel_hi:[1,0]
	v_pk_mul_f32 v[42:43], v[42:43], v[198:199] op_sel_hi:[1,0]
	v_pk_mul_f32 v[44:45], v[44:45], v[198:199] op_sel_hi:[1,0]
	v_pk_mul_f32 v[38:39], v[38:39], v[198:199] op_sel_hi:[1,0]
	v_pk_mul_f32 v[40:41], v[40:41], v[198:199] op_sel_hi:[1,0]
	v_pk_mul_f32 v[30:31], v[30:31], v[198:199] op_sel_hi:[1,0]
	v_pk_mul_f32 v[32:33], v[32:33], v[198:199] op_sel_hi:[1,0]
	v_cvt_pk_bf16_f32 v50, v50, v51
	v_cvt_pk_bf16_f32 v51, v52, v53
	v_cvt_pk_bf16_f32 v52, v42, v43
	v_cvt_pk_bf16_f32 v53, v44, v45
	v_cvt_pk_bf16_f32 v38, v38, v39
	v_cvt_pk_bf16_f32 v39, v40, v41
	v_cvt_pk_bf16_f32 v40, v30, v31
	v_cvt_pk_bf16_f32 v41, v32, v33
	ds_bpermute_b32 v42, v166, v50
	ds_bpermute_b32 v43, v166, v51
	ds_bpermute_b32 v44, v166, v52
	ds_bpermute_b32 v45, v166, v53
	ds_bpermute_b32 v30, v166, v38
	ds_bpermute_b32 v31, v166, v39
	ds_bpermute_b32 v32, v166, v40
	ds_bpermute_b32 v33, v166, v41
	v_add_co_u32_e32 v212, vcc, 0xd8000, v208
	v_addc_co_u32_e32 v213, vcc, 0, v209, vcc
	s_waitcnt lgkmcnt(8)
	global_store_dwordx4 v[210:211], v[58:61], off
	global_store_dwordx4 v[210:211], v[46:49], off offset:256
	v_pk_mul_f32 v[34:35], v[34:35], v[202:203] op_sel_hi:[1,0]
	v_pk_mul_f32 v[36:37], v[36:37], v[202:203] op_sel_hi:[1,0]
	v_pk_mul_f32 v[26:27], v[26:27], v[202:203] op_sel_hi:[1,0]
	v_pk_mul_f32 v[28:29], v[28:29], v[202:203] op_sel_hi:[1,0]
	v_pk_mul_f32 v[22:23], v[22:23], v[202:203] op_sel_hi:[1,0]
	v_pk_mul_f32 v[24:25], v[24:25], v[202:203] op_sel_hi:[1,0]
	v_pk_mul_f32 v[14:15], v[14:15], v[202:203] op_sel_hi:[1,0]
	v_pk_mul_f32 v[16:17], v[16:17], v[202:203] op_sel_hi:[1,0]
	v_cvt_pk_bf16_f32 v34, v34, v35
	v_cvt_pk_bf16_f32 v35, v36, v37
	v_cvt_pk_bf16_f32 v36, v26, v27
	v_cvt_pk_bf16_f32 v37, v28, v29
	v_cvt_pk_bf16_f32 v22, v22, v23
	v_cvt_pk_bf16_f32 v23, v24, v25
	v_cvt_pk_bf16_f32 v24, v14, v15
	v_cvt_pk_bf16_f32 v25, v16, v17
	ds_bpermute_b32 v26, v166, v34
	ds_bpermute_b32 v27, v166, v35
	ds_bpermute_b32 v28, v166, v36
	ds_bpermute_b32 v29, v166, v37
	ds_bpermute_b32 v14, v166, v22
	ds_bpermute_b32 v15, v166, v23
	ds_bpermute_b32 v16, v166, v24
	ds_bpermute_b32 v17, v166, v25
	v_add_co_u32_e32 v210, vcc, 0xf0000, v208
	v_addc_co_u32_e32 v211, vcc, 0, v209, vcc
	s_waitcnt lgkmcnt(8)
	global_store_dwordx4 v[212:213], v[42:45], off
	global_store_dwordx4 v[212:213], v[30:33], off offset:256
	v_pk_mul_f32 v[18:19], v[18:19], v[206:207] op_sel_hi:[1,0]
	v_pk_mul_f32 v[20:21], v[20:21], v[206:207] op_sel_hi:[1,0]
	v_pk_mul_f32 v[10:11], v[10:11], v[206:207] op_sel_hi:[1,0]
	v_pk_mul_f32 v[12:13], v[12:13], v[206:207] op_sel_hi:[1,0]
	v_pk_mul_f32 v[6:7], v[6:7], v[206:207] op_sel_hi:[1,0]
	v_pk_mul_f32 v[8:9], v[8:9], v[206:207] op_sel_hi:[1,0]
	v_pk_mul_f32 v[2:3], v[2:3], v[206:207] op_sel_hi:[1,0]
	v_pk_mul_f32 v[4:5], v[4:5], v[206:207] op_sel_hi:[1,0]
	v_cvt_pk_bf16_f32 v18, v18, v19
	v_cvt_pk_bf16_f32 v19, v20, v21
	v_cvt_pk_bf16_f32 v20, v10, v11
	v_cvt_pk_bf16_f32 v21, v12, v13
	v_cvt_pk_bf16_f32 v6, v6, v7
	v_cvt_pk_bf16_f32 v7, v8, v9
	v_cvt_pk_bf16_f32 v8, v2, v3
	v_cvt_pk_bf16_f32 v9, v4, v5
	ds_bpermute_b32 v10, v166, v18
	ds_bpermute_b32 v11, v166, v19
	ds_bpermute_b32 v12, v166, v20
	ds_bpermute_b32 v13, v166, v21
	ds_bpermute_b32 v2, v166, v6
	ds_bpermute_b32 v3, v166, v7
	ds_bpermute_b32 v4, v166, v8
	ds_bpermute_b32 v5, v166, v9
	v_add_co_u32_e32 v212, vcc, 0x108000, v208
	v_addc_co_u32_e32 v213, vcc, 0, v209, vcc
	s_waitcnt lgkmcnt(8)
	global_store_dwordx4 v[210:211], v[26:29], off
	global_store_dwordx4 v[210:211], v[14:17], off offset:256
	s_waitcnt lgkmcnt(0)
	global_store_dwordx4 v[212:213], v[10:13], off
	global_store_dwordx4 v[212:213], v[2:5], off offset:256
	s_setprio 0
	s_andn2_b64 vcc, exec, s[4:5]
	s_mov_b64 s[4:5], -1
	s_cbranch_vccnz .LBB0_249
	s_andn2_b64 vcc, exec, s[6:7]
	s_cbranch_vccnz .LBB0_248
	s_barrier
	s_branch .LBB0_248

; __device__ __forceinline__ void rstd8(const float* SS, int rowb, int lane, float (&rs)[2][4]) {
;     f32x4 p[2][4];
; #pragma unroll
;     for (int ai = 0; ai < 2; ++ai)
; #pragma unroll
;         for (int m = 0; m < 4; ++m) p[ai][m] = *(const f32x4*)(SS + (size_t)(rowb + HALF * ai + 16 * m + (lane >> 2)) * 16 + 4 * (lane & 3));
;     asm volatile("" : "+v"(p[0][0]), "+v"(p[0][1]), "+v"(p[0][2]), "+v"(p[0][3]), "+v"(p[1][0]), "+v"(p[1][1]), "+v"(p[1][2]), "+v"(p[1][3]));
; #pragma unroll
;     for (int ai = 0; ai < 2; ++ai)
; #pragma unroll
;     __device__ __forceinline__ void operator()(const f32x4 (&acc)[2][2][4][2], const Unit& u, int wr, int wc, int fr, int fq) const {
;         const int row0 = u.pm * BM + wr * 64 + fr; const int pnl = MOE ? (u.pn % 28) : u.pn;
;         const int lane = fr + 16 * fq, qs4 = QSRC_ST(lane); const int rowS = u.pm * BM + wr * 64 + (lane >> 2), colS = pnl * HALF + wc * 32 + 8 * (lane & 3);
;         float rs8[2][4];
;         if constexpr (MOE) {
; #pragma unroll
;             for (int ai = 0; ai < 2; ++ai)
; #pragma unroll
;                 for (int m = 0; m < 4; ++m) rs8[ai][m] = SS[row0 + ai * HALF + m * 16];
;             asm volatile("" : "+v"(rs8[0][0]), "+v"(rs8[0][1]), "+v"(rs8[0][2]), "+v"(rs8[0][3]), "+v"(rs8[1][0]), "+v"(rs8[1][1]), "+v"(rs8[1][2]), "+v"(rs8[1][3]));
;         } else rstd8(SS, u.pm * BM + wr * 64, lane, rs8);
; #pragma unroll
;         for (int ai = 0; ai < 2; ++ai) {
; #pragma unroll
;             for (int m = 0; m < 4; ++m) { const int row = row0 + ai * HALF + m * 16; const float rs = rs8[ai][m];
;                 const f32x4 a0 = acc[ai][0][m][0] * rs, a1 = acc[ai][0][m][1] * rs, b0 = acc[ai][1][m][0] * rs, b1 = acc[ai][1][m][1] * rs;
;                 f32x4 g0, g1;
; #pragma unroll
;                 for (int j = 0; j < 4; ++j) { g0[j] = silu_f(a0[j]) * b0[j]; g1[j] = silu_f(a1[j]) * b1[j]; }
;                 u32x4 w; w.x = cvt_pk_bf16(g0[0], g0[1]); w.y = cvt_pk_bf16(g0[2], g0[3]); w.z = cvt_pk_bf16(g1[0], g1[1]); w.w = cvt_pk_bf16(g1[2], g1[3]);
;                 w = lane_perm(w, qs4); u32x4* dst = (u32x4*)(O + (size_t)(rowS + ai * HALF + m * 16) * ldo + colS); (void)row;
;                 if constexpr (MOE) __builtin_nontemporal_store(w, dst); else *dst = w; } }
.LBB0_724:
	s_and_b64 vcc, exec, s[10:11]
	s_cbranch_vccz .Lepi_prio1
	s_setprio 2
.Lepi_prio1:
	v_lshl_add_u32 v182, s20, 8, v175
	v_ashrrev_i32_e32 v183, 31, v182
	v_lshlrev_b64 v[130:131], 6, v[182:183]
	v_lshl_add_u64 v[130:131], v[150:151], 0, v[130:131]
	v_add_co_u32_e32 v132, vcc, 0x2000, v130
	v_addc_co_u32_e32 v133, vcc, 0, v131, vcc
	global_load_dwordx4 v[208:211], v[132:133], off
	global_load_dwordx4 v[212:215], v[132:133], off offset:1024
	global_load_dwordx4 v[216:219], v[132:133], off offset:2048
	global_load_dwordx4 v[220:223], v[132:133], off offset:3072
	v_add_f32_e32 v238, v238, v239
	v_add_f32_e32 v242, v242, v243
	v_add_f32_e32 v246, v246, v247
	v_add_f32_e32 v250, v250, v251
	v_add_f32_e32 v240, v240, v241
	v_add_f32_e32 v244, v244, v245
	v_add_f32_e32 v248, v248, v249
	v_add_f32_e32 v252, v252, v253
	v_add_f32_e32 v238, v238, v240
	v_add_f32_e32 v242, v242, v244
	v_add_f32_e32 v246, v246, v248
	v_add_f32_e32 v250, v250, v252
	v_add_f32_dpp v238, v238, v238 quad_perm:[1,0,3,2] row_mask:0xf bank_mask:0xf
	v_add_f32_dpp v242, v242, v242 quad_perm:[1,0,3,2] row_mask:0xf bank_mask:0xf
	v_add_f32_dpp v246, v246, v246 quad_perm:[1,0,3,2] row_mask:0xf bank_mask:0xf
	v_add_f32_dpp v250, v250, v250 quad_perm:[1,0,3,2] row_mask:0xf bank_mask:0xf
	v_add_f32_dpp v238, v238, v238 quad_perm:[2,3,0,1] row_mask:0xf bank_mask:0xf
	v_add_f32_dpp v242, v242, v242 quad_perm:[2,3,0,1] row_mask:0xf bank_mask:0xf
	v_add_f32_dpp v246, v246, v246 quad_perm:[2,3,0,1] row_mask:0xf bank_mask:0xf
	v_add_f32_dpp v250, v250, v250 quad_perm:[2,3,0,1] row_mask:0xf bank_mask:0xf
	v_fmamk_f32 v238, v238, 0x3a800000, v190
	v_fmamk_f32 v242, v242, 0x3a800000, v190
	v_fmamk_f32 v246, v246, 0x3a800000, v190
	v_fmamk_f32 v250, v250, 0x3a800000, v190
	ds_bpermute_b32 v238, v179, v238
	ds_bpermute_b32 v242, v179, v242
	ds_bpermute_b32 v246, v179, v246
	ds_bpermute_b32 v250, v179, v250
	v_lshl_or_b32 v184, s21, 7, v181
	v_ashrrev_i32_e32 v185, 31, v184
	v_mov_b64_e32 v[134:135], s[44:45]
	v_lshlrev_b64 v[184:185], 1, v[184:185]
	v_mad_i64_i32 v[224:225], s[20:21], v182, s49, v[134:135]
	s_nop 0
	v_lshl_add_u64 v[224:225], v[224:225], 0, v[184:185]
	v_pk_mul_f32 v[118:119], v[118:119], v[126:127]
	v_pk_mul_f32 v[120:121], v[120:121], v[128:129]
	v_pk_mul_f32 v[114:115], v[114:115], v[122:123]
	v_pk_mul_f32 v[116:117], v[116:117], v[124:125]
	v_pk_mul_f32 v[102:103], v[102:103], v[110:111]
	v_pk_mul_f32 v[104:105], v[104:105], v[112:113]
	v_pk_mul_f32 v[98:99], v[98:99], v[106:107]
	v_pk_mul_f32 v[100:101], v[100:101], v[108:109]
	v_pk_mul_f32 v[86:87], v[86:87], v[94:95]
	v_pk_mul_f32 v[88:89], v[88:89], v[96:97]
	v_pk_mul_f32 v[82:83], v[82:83], v[90:91]
	v_pk_mul_f32 v[84:85], v[84:85], v[92:93]
	v_pk_mul_f32 v[70:71], v[70:71], v[78:79]
	v_pk_mul_f32 v[72:73], v[72:73], v[80:81]
	v_pk_mul_f32 v[66:67], v[66:67], v[74:75]
	v_pk_mul_f32 v[68:69], v[68:69], v[76:77]
	v_pk_mul_f32 v[54:55], v[54:55], v[62:63]
	v_pk_mul_f32 v[56:57], v[56:57], v[64:65]
	v_pk_mul_f32 v[50:51], v[50:51], v[58:59]
	v_pk_mul_f32 v[52:53], v[52:53], v[60:61]
	v_pk_mul_f32 v[38:39], v[38:39], v[46:47]
	v_pk_mul_f32 v[40:41], v[40:41], v[48:49]
	v_pk_mul_f32 v[34:35], v[34:35], v[42:43]
	v_pk_mul_f32 v[36:37], v[36:37], v[44:45]
	v_pk_mul_f32 v[22:23], v[22:23], v[30:31]
	v_pk_mul_f32 v[24:25], v[24:25], v[32:33]
	v_pk_mul_f32 v[18:19], v[18:19], v[26:27]
	v_pk_mul_f32 v[20:21], v[20:21], v[28:29]
	v_pk_mul_f32 v[6:7], v[6:7], v[14:15]
	v_pk_mul_f32 v[8:9], v[8:9], v[16:17]
	v_pk_mul_f32 v[2:3], v[2:3], v[10:11]
	v_pk_mul_f32 v[4:5], v[4:5], v[12:13]
	s_waitcnt lgkmcnt(0)
	v_rsq_f32_e32 v240, v238
	v_rsq_f32_e32 v244, v242
	v_rsq_f32_e32 v248, v246
	v_rsq_f32_e32 v252, v250
	s_nop 0
	v_mul_f32_e32 v240, 0xbfb8aa3b, v240
	v_mul_f32_e32 v244, 0xbfb8aa3b, v244
	v_mul_f32_e32 v248, 0xbfb8aa3b, v248
	v_mul_f32_e32 v252, 0xbfb8aa3b, v252
	v_pk_mul_f32 v[126:127], v[126:127], v[240:241] op_sel_hi:[1,0]
	v_pk_mul_f32 v[128:129], v[128:129], v[240:241] op_sel_hi:[1,0]
	v_pk_mul_f32 v[122:123], v[122:123], v[240:241] op_sel_hi:[1,0]
	v_pk_mul_f32 v[124:125], v[124:125], v[240:241] op_sel_hi:[1,0]
	v_exp_f32_e32 v126, v126
	v_exp_f32_e32 v127, v127
	v_exp_f32_e32 v128, v128
	v_exp_f32_e32 v129, v129
	v_exp_f32_e32 v122, v122
	v_exp_f32_e32 v123, v123
	v_exp_f32_e32 v124, v124
	v_exp_f32_e32 v125, v125
	v_pk_fma_f32 v[126:127], v[126:127], v[238:239], v[238:239] op_sel_hi:[1,0,0]
	v_pk_fma_f32 v[128:129], v[128:129], v[238:239], v[238:239] op_sel_hi:[1,0,0]
	v_pk_fma_f32 v[122:123], v[122:123], v[238:239], v[238:239] op_sel_hi:[1,0,0]
	v_pk_fma_f32 v[124:125], v[124:125], v[238:239], v[238:239] op_sel_hi:[1,0,0]
	v_rcp_f32_e32 v126, v126
	v_rcp_f32_e32 v127, v127
	v_rcp_f32_e32 v128, v128
	v_rcp_f32_e32 v129, v129
	v_rcp_f32_e32 v122, v122
	v_rcp_f32_e32 v123, v123
	v_rcp_f32_e32 v124, v124
	v_rcp_f32_e32 v125, v125
	v_pk_mul_f32 v[118:119], v[118:119], v[126:127]
	v_pk_mul_f32 v[120:121], v[120:121], v[128:129]
	v_pk_mul_f32 v[114:115], v[114:115], v[122:123]
	v_pk_mul_f32 v[116:117], v[116:117], v[124:125]
	v_cvt_pk_bf16_f32 v126, v118, v119
	v_cvt_pk_bf16_f32 v127, v120, v121
	v_cvt_pk_bf16_f32 v128, v114, v115
	v_cvt_pk_bf16_f32 v129, v116, v117
	ds_bpermute_b32 v122, v171, v126
	ds_bpermute_b32 v123, v171, v127
	ds_bpermute_b32 v124, v171, v128
	ds_bpermute_b32 v125, v171, v129
	v_mov_b32_e32 v226, v224
	v_mov_b32_e32 v227, v225
	v_pk_mul_f32 v[110:111], v[110:111], v[244:245] op_sel_hi:[1,0]
	v_pk_mul_f32 v[112:113], v[112:113], v[244:245] op_sel_hi:[1,0]
	v_pk_mul_f32 v[106:107], v[106:107], v[244:245] op_sel_hi:[1,0]
	v_pk_mul_f32 v[108:109], v[108:109], v[244:245] op_sel_hi:[1,0]
	v_exp_f32_e32 v110, v110
	v_exp_f32_e32 v111, v111
	v_exp_f32_e32 v112, v112
	v_exp_f32_e32 v113, v113
	v_exp_f32_e32 v106, v106
	v_exp_f32_e32 v107, v107
	v_exp_f32_e32 v108, v108
	v_exp_f32_e32 v109, v109
	v_pk_fma_f32 v[110:111], v[110:111], v[242:243], v[242:243] op_sel_hi:[1,0,0]
	v_pk_fma_f32 v[112:113], v[112:113], v[242:243], v[242:243] op_sel_hi:[1,0,0]
	v_pk_fma_f32 v[106:107], v[106:107], v[242:243], v[242:243] op_sel_hi:[1,0,0]
	v_pk_fma_f32 v[108:109], v[108:109], v[242:243], v[242:243] op_sel_hi:[1,0,0]
	v_rcp_f32_e32 v110, v110
	v_rcp_f32_e32 v111, v111
	v_rcp_f32_e32 v112, v112
	v_rcp_f32_e32 v113, v113
	v_rcp_f32_e32 v106, v106
	v_rcp_f32_e32 v107, v107
	v_rcp_f32_e32 v108, v108
	v_rcp_f32_e32 v109, v109
	v_pk_mul_f32 v[102:103], v[102:103], v[110:111]
	v_pk_mul_f32 v[104:105], v[104:105], v[112:113]
	v_pk_mul_f32 v[98:99], v[98:99], v[106:107]
	v_pk_mul_f32 v[100:101], v[100:101], v[108:109]
	s_waitcnt lgkmcnt(0)
; __device__ __forceinline__ unsigned cvt_pk_bf16(float lo, float hi) { const f32x2c_t v = {lo, hi}; return __builtin_bit_cast(unsigned, __builtin_convertvector(v, bf16x2c_t)); }
; __device__ __forceinline__ float silu_f(float a) { return a * __builtin_amdgcn_rcpf(1.0f + __builtin_amdgcn_exp2f(a * -1.4426950408889634f)); }
; __device__ __forceinline__ void rstd8(const float* SS, int rowb, int lane, float (&rs)[2][4]) {
;     ...
;         for (int m = 0; m < 4; ++m) p[ai][m] = *(const f32x4*)(SS + (size_t)(rowb + HALF * ai + 16 * m + (lane >> 2)) * 16 + 4 * (lane & 3));
;     asm volatile("" : "+v"(p[0][0]), "+v"(p[0][1]), "+v"(p[0][2]), "+v"(p[0][3]), "+v"(p[1][0]), "+v"(p[1][1]), "+v"(p[1][2]), "+v"(p[1][3]));
; #pragma unroll
;     for (int ai = 0; ai < 2; ++ai)
; #pragma unroll
;         for (int m = 0; m < 4; ++m) { float s = (p[ai][m][0] + p[ai][m][1]) + (p[ai][m][2] + p[ai][m][3]); s += __shfl_xor(s, 1); s += __shfl_xor(s, 2);
;             const float r = __builtin_amdgcn_rsqf(s * (1.0f / 1024.0f) + RMS_EPS);
;             rs[ai][m] = __builtin_bit_cast(float, __builtin_amdgcn_ds_bpermute((lane & 15) << 4, __builtin_bit_cast(int, r))); }
;     __device__ __forceinline__ void operator()(const f32x4 (&acc)[2][2][4][2], const Unit& u, int wr, int wc, int fr, int fq) const {
;     ...
;         for (int ai = 0; ai < 2; ++ai) {
; #pragma unroll
;             for (int m = 0; m < 4; ++m) { const int row = row0 + ai * HALF + m * 16; const float rs = rs8[ai][m];
;                 const f32x4 a0 = acc[ai][0][m][0] * rs, a1 = acc[ai][0][m][1] * rs, b0 = acc[ai][1][m][0] * rs, b1 = acc[ai][1][m][1] * rs;
;                 f32x4 g0, g1;
; #pragma unroll
;                 for (int j = 0; j < 4; ++j) { g0[j] = silu_f(a0[j]) * b0[j]; g1[j] = silu_f(a1[j]) * b1[j]; }
;                 u32x4 w; w.x = cvt_pk_bf16(g0[0], g0[1]); w.y = cvt_pk_bf16(g0[2], g0[3]); w.z = cvt_pk_bf16(g1[0], g1[1]); w.w = cvt_pk_bf16(g1[2], g1[3]);
;                 w = lane_perm(w, qs4); u32x4* dst = (u32x4*)(O + (size_t)(rowS + ai * HALF + m * 16) * ldo + colS); (void)row;
;                 if constexpr (MOE) __builtin_nontemporal_store(w, dst); else *dst = w; } }
	global_store_dwordx4 v[226:227], v[122:125], off
	v_cvt_pk_bf16_f32 v110, v102, v103
	v_cvt_pk_bf16_f32 v111, v104, v105
	v_cvt_pk_bf16_f32 v112, v98, v99
	v_cvt_pk_bf16_f32 v113, v100, v101
	ds_bpermute_b32 v106, v171, v110
	ds_bpermute_b32 v107, v171, v111
	ds_bpermute_b32 v108, v171, v112
	ds_bpermute_b32 v109, v171, v113
	v_add_co_u32_e32 v230, vcc, 0x16000, v224
	v_addc_co_u32_e32 v231, vcc, 0, v225, vcc
	v_pk_mul_f32 v[94:95], v[94:95], v[248:249] op_sel_hi:[1,0]
	v_pk_mul_f32 v[96:97], v[96:97], v[248:249] op_sel_hi:[1,0]
	v_pk_mul_f32 v[90:91], v[90:91], v[248:249] op_sel_hi:[1,0]
	v_pk_mul_f32 v[92:93], v[92:93], v[248:249] op_sel_hi:[1,0]
	v_exp_f32_e32 v94, v94
	v_exp_f32_e32 v95, v95
	v_exp_f32_e32 v96, v96
	v_exp_f32_e32 v97, v97
	v_exp_f32_e32 v90, v90
	v_exp_f32_e32 v91, v91
	v_exp_f32_e32 v92, v92
	v_exp_f32_e32 v93, v93
	v_pk_fma_f32 v[94:95], v[94:95], v[246:247], v[246:247] op_sel_hi:[1,0,0]
	v_pk_fma_f32 v[96:97], v[96:97], v[246:247], v[246:247] op_sel_hi:[1,0,0]
	v_pk_fma_f32 v[90:91], v[90:91], v[246:247], v[246:247] op_sel_hi:[1,0,0]
	v_pk_fma_f32 v[92:93], v[92:93], v[246:247], v[246:247] op_sel_hi:[1,0,0]
	v_rcp_f32_e32 v94, v94
	v_rcp_f32_e32 v95, v95
	v_rcp_f32_e32 v96, v96
	v_rcp_f32_e32 v97, v97
	v_rcp_f32_e32 v90, v90
	v_rcp_f32_e32 v91, v91
	v_rcp_f32_e32 v92, v92
	v_rcp_f32_e32 v93, v93
	v_pk_mul_f32 v[86:87], v[86:87], v[94:95]
	v_pk_mul_f32 v[88:89], v[88:89], v[96:97]
	v_pk_mul_f32 v[82:83], v[82:83], v[90:91]
	v_pk_mul_f32 v[84:85], v[84:85], v[92:93]
	s_waitcnt lgkmcnt(0)
	global_store_dwordx4 v[230:231], v[106:109], off
	v_cvt_pk_bf16_f32 v94, v86, v87
	v_cvt_pk_bf16_f32 v95, v88, v89
	v_cvt_pk_bf16_f32 v96, v82, v83
	v_cvt_pk_bf16_f32 v97, v84, v85
	ds_bpermute_b32 v90, v171, v94
	ds_bpermute_b32 v91, v171, v95
	ds_bpermute_b32 v92, v171, v96
	ds_bpermute_b32 v93, v171, v97
	v_add_co_u32_e32 v226, vcc, 0x2c000, v224
	v_addc_co_u32_e32 v227, vcc, 0, v225, vcc
	v_pk_mul_f32 v[78:79], v[78:79], v[252:253] op_sel_hi:[1,0]
	v_pk_mul_f32 v[80:81], v[80:81], v[252:253] op_sel_hi:[1,0]
	v_pk_mul_f32 v[74:75], v[74:75], v[252:253] op_sel_hi:[1,0]
	v_pk_mul_f32 v[76:77], v[76:77], v[252:253] op_sel_hi:[1,0]
	v_exp_f32_e32 v78, v78
	v_exp_f32_e32 v79, v79
	v_exp_f32_e32 v80, v80
	v_exp_f32_e32 v81, v81
	v_exp_f32_e32 v74, v74
	v_exp_f32_e32 v75, v75
	v_exp_f32_e32 v76, v76
	v_exp_f32_e32 v77, v77
	v_pk_fma_f32 v[78:79], v[78:79], v[250:251], v[250:251] op_sel_hi:[1,0,0]
	v_pk_fma_f32 v[80:81], v[80:81], v[250:251], v[250:251] op_sel_hi:[1,0,0]
	v_pk_fma_f32 v[74:75], v[74:75], v[250:251], v[250:251] op_sel_hi:[1,0,0]
	v_pk_fma_f32 v[76:77], v[76:77], v[250:251], v[250:251] op_sel_hi:[1,0,0]
	v_rcp_f32_e32 v78, v78
	v_rcp_f32_e32 v79, v79
	v_rcp_f32_e32 v80, v80
	v_rcp_f32_e32 v81, v81
	v_rcp_f32_e32 v74, v74
	v_rcp_f32_e32 v75, v75
	v_rcp_f32_e32 v76, v76
	v_rcp_f32_e32 v77, v77
	v_pk_mul_f32 v[70:71], v[70:71], v[78:79]
	v_pk_mul_f32 v[72:73], v[72:73], v[80:81]
	v_pk_mul_f32 v[66:67], v[66:67], v[74:75]
	v_pk_mul_f32 v[68:69], v[68:69], v[76:77]
	s_waitcnt lgkmcnt(0)
	global_store_dwordx4 v[226:227], v[90:93], off
	v_cvt_pk_bf16_f32 v78, v70, v71
	v_cvt_pk_bf16_f32 v79, v72, v73
	v_cvt_pk_bf16_f32 v80, v66, v67
	v_cvt_pk_bf16_f32 v81, v68, v69
	ds_bpermute_b32 v74, v171, v78
	ds_bpermute_b32 v75, v171, v79
	ds_bpermute_b32 v76, v171, v80
	ds_bpermute_b32 v77, v171, v81
	v_add_co_u32_e32 v230, vcc, 0x42000, v224
	v_addc_co_u32_e32 v231, vcc, 0, v225, vcc
	s_waitcnt vmcnt(3)
	v_add_f32_e32 v208, v208, v209
	v_add_f32_e32 v212, v212, v213
	v_add_f32_e32 v216, v216, v217
	v_add_f32_e32 v220, v220, v221
	v_add_f32_e32 v210, v210, v211
	v_add_f32_e32 v214, v214, v215
	v_add_f32_e32 v218, v218, v219
	v_add_f32_e32 v222, v222, v223
	v_add_f32_e32 v208, v208, v210
	v_add_f32_e32 v212, v212, v214
	v_add_f32_e32 v216, v216, v218
	v_add_f32_e32 v220, v220, v222
	v_add_f32_dpp v208, v208, v208 quad_perm:[1,0,3,2] row_mask:0xf bank_mask:0xf
	v_add_f32_dpp v212, v212, v212 quad_perm:[1,0,3,2] row_mask:0xf bank_mask:0xf
	v_add_f32_dpp v216, v216, v216 quad_perm:[1,0,3,2] row_mask:0xf bank_mask:0xf
	v_add_f32_dpp v220, v220, v220 quad_perm:[1,0,3,2] row_mask:0xf bank_mask:0xf
	v_add_f32_dpp v208, v208, v208 quad_perm:[2,3,0,1] row_mask:0xf bank_mask:0xf
	v_add_f32_dpp v212, v212, v212 quad_perm:[2,3,0,1] row_mask:0xf bank_mask:0xf
	v_add_f32_dpp v216, v216, v216 quad_perm:[2,3,0,1] row_mask:0xf bank_mask:0xf
	v_add_f32_dpp v220, v220, v220 quad_perm:[2,3,0,1] row_mask:0xf bank_mask:0xf
	v_fmamk_f32 v208, v208, 0x3a800000, v190
	v_fmamk_f32 v212, v212, 0x3a800000, v190
	v_fmamk_f32 v216, v216, 0x3a800000, v190
	v_fmamk_f32 v220, v220, 0x3a800000, v190
	ds_bpermute_b32 v208, v179, v208
	ds_bpermute_b32 v212, v179, v212
	ds_bpermute_b32 v216, v179, v216
	ds_bpermute_b32 v220, v179, v220
	s_waitcnt lgkmcnt(0)
; __device__ __forceinline__ unsigned cvt_pk_bf16(float lo, float hi) { const f32x2c_t v = {lo, hi}; return __builtin_bit_cast(unsigned, __builtin_convertvector(v, bf16x2c_t)); }
; __device__ __forceinline__ float silu_f(float a) { return a * __builtin_amdgcn_rcpf(1.0f + __builtin_amdgcn_exp2f(a * -1.4426950408889634f)); }
; #define PG8_BAR __builtin_amdgcn_s_barrier()
;     __device__ __forceinline__ void operator()(const f32x4 (&acc)[2][2][4][2], const Unit& u, int wr, int wc, int fr, int fq) const {
;     ...
;         for (int ai = 0; ai < 2; ++ai) {
; #pragma unroll
;             for (int m = 0; m < 4; ++m) { const int row = row0 + ai * HALF + m * 16; const float rs = rs8[ai][m];
;                 const f32x4 a0 = acc[ai][0][m][0] * rs, a1 = acc[ai][0][m][1] * rs, b0 = acc[ai][1][m][0] * rs, b1 = acc[ai][1][m][1] * rs;
;                 f32x4 g0, g1;
; #pragma unroll
;                 for (int j = 0; j < 4; ++j) { g0[j] = silu_f(a0[j]) * b0[j]; g1[j] = silu_f(a1[j]) * b1[j]; }
;                 u32x4 w; w.x = cvt_pk_bf16(g0[0], g0[1]); w.y = cvt_pk_bf16(g0[2], g0[3]); w.z = cvt_pk_bf16(g1[0], g1[1]); w.w = cvt_pk_bf16(g1[2], g1[3]);
;                 w = lane_perm(w, qs4); u32x4* dst = (u32x4*)(O + (size_t)(rowS + ai * HALF + m * 16) * ldo + colS); (void)row;
;                 if constexpr (MOE) __builtin_nontemporal_store(w, dst); else *dst = w; } }
; template <class Epi, class Sched, bool ALIGN_EPI = false, bool SP2 = false>
; __device__ __forceinline__ void gemm_phase(PG8_LAS unsigned char* lds, const Gemm g, const Sched& S, const Epi& E, const bool skip_epi = false) {
;     ...
;         if constexpr (!Epi::AFTER_DRAIN) { if (!skip_epi) E(acc, cur, wr, wc, fr, fq); S.done(cur); }
;         if (!has_next) break;
; #pragma unroll
;         for (int a = 0; a < 2; ++a)
; #pragma unroll
;             for (int b = 0; b < 2; ++b)
; #pragma unroll
;                 for (int m = 0; m < 4; ++m)
; #pragma unroll
;                     for (int n = 0; n < 2; ++n) acc[a][b][m][n] = (f32x4){0.f, 0.f, 0.f, 0.f};
;         cur = nxt; cA = nA; cB = nB; ++ui;
;         if constexpr (Sched::GATHER) { gA[0][0] = gN[0][0]; gA[0][1] = gN[0][1]; gA[1][0] = gN[1][0]; gA[1][1] = gN[1][1]; }
;         if constexpr (ALIGN_EPI) { if (wr == 1) PG8_BAR; }
	global_store_dwordx4 v[230:231], v[74:77], off
	v_rsq_f32_e32 v210, v208
	v_rsq_f32_e32 v214, v212
	v_rsq_f32_e32 v218, v216
	v_rsq_f32_e32 v222, v220
	s_nop 0
	v_mul_f32_e32 v210, 0xbfb8aa3b, v210
	v_mul_f32_e32 v214, 0xbfb8aa3b, v214
	v_mul_f32_e32 v218, 0xbfb8aa3b, v218
	v_mul_f32_e32 v222, 0xbfb8aa3b, v222
	v_pk_mul_f32 v[62:63], v[62:63], v[210:211] op_sel_hi:[1,0]
	v_pk_mul_f32 v[64:65], v[64:65], v[210:211] op_sel_hi:[1,0]
	v_pk_mul_f32 v[58:59], v[58:59], v[210:211] op_sel_hi:[1,0]
	v_pk_mul_f32 v[60:61], v[60:61], v[210:211] op_sel_hi:[1,0]
	v_exp_f32_e32 v62, v62
	v_exp_f32_e32 v63, v63
	v_exp_f32_e32 v64, v64
	v_exp_f32_e32 v65, v65
	v_exp_f32_e32 v58, v58
	v_exp_f32_e32 v59, v59
	v_exp_f32_e32 v60, v60
	v_exp_f32_e32 v61, v61
	v_pk_fma_f32 v[62:63], v[62:63], v[208:209], v[208:209] op_sel_hi:[1,0,0]
	v_pk_fma_f32 v[64:65], v[64:65], v[208:209], v[208:209] op_sel_hi:[1,0,0]
	v_pk_fma_f32 v[58:59], v[58:59], v[208:209], v[208:209] op_sel_hi:[1,0,0]
	v_pk_fma_f32 v[60:61], v[60:61], v[208:209], v[208:209] op_sel_hi:[1,0,0]
	v_rcp_f32_e32 v62, v62
	v_rcp_f32_e32 v63, v63
	v_rcp_f32_e32 v64, v64
	v_rcp_f32_e32 v65, v65
	v_rcp_f32_e32 v58, v58
	v_rcp_f32_e32 v59, v59
	v_rcp_f32_e32 v60, v60
	v_rcp_f32_e32 v61, v61
	v_pk_mul_f32 v[54:55], v[54:55], v[62:63]
	v_pk_mul_f32 v[56:57], v[56:57], v[64:65]
	v_pk_mul_f32 v[50:51], v[50:51], v[58:59]
	v_pk_mul_f32 v[52:53], v[52:53], v[60:61]
	v_cvt_pk_bf16_f32 v62, v54, v55
	v_cvt_pk_bf16_f32 v63, v56, v57
	v_cvt_pk_bf16_f32 v64, v50, v51
	v_cvt_pk_bf16_f32 v65, v52, v53
	ds_bpermute_b32 v58, v171, v62
	ds_bpermute_b32 v59, v171, v63
	ds_bpermute_b32 v60, v171, v64
	ds_bpermute_b32 v61, v171, v65
	v_add_co_u32_e32 v226, vcc, 0xb0000, v224
	v_addc_co_u32_e32 v227, vcc, 0, v225, vcc
	v_pk_mul_f32 v[46:47], v[46:47], v[214:215] op_sel_hi:[1,0]
	v_pk_mul_f32 v[48:49], v[48:49], v[214:215] op_sel_hi:[1,0]
	v_pk_mul_f32 v[42:43], v[42:43], v[214:215] op_sel_hi:[1,0]
	v_pk_mul_f32 v[44:45], v[44:45], v[214:215] op_sel_hi:[1,0]
	v_exp_f32_e32 v46, v46
	v_exp_f32_e32 v47, v47
	v_exp_f32_e32 v48, v48
	v_exp_f32_e32 v49, v49
	v_exp_f32_e32 v42, v42
	v_exp_f32_e32 v43, v43
	v_exp_f32_e32 v44, v44
	v_exp_f32_e32 v45, v45
	v_pk_fma_f32 v[46:47], v[46:47], v[212:213], v[212:213] op_sel_hi:[1,0,0]
	v_pk_fma_f32 v[48:49], v[48:49], v[212:213], v[212:213] op_sel_hi:[1,0,0]
	v_pk_fma_f32 v[42:43], v[42:43], v[212:213], v[212:213] op_sel_hi:[1,0,0]
	v_pk_fma_f32 v[44:45], v[44:45], v[212:213], v[212:213] op_sel_hi:[1,0,0]
	v_rcp_f32_e32 v46, v46
	v_rcp_f32_e32 v47, v47
	v_rcp_f32_e32 v48, v48
	v_rcp_f32_e32 v49, v49
	v_rcp_f32_e32 v42, v42
	v_rcp_f32_e32 v43, v43
	v_rcp_f32_e32 v44, v44
	v_rcp_f32_e32 v45, v45
	v_pk_mul_f32 v[38:39], v[38:39], v[46:47]
	v_pk_mul_f32 v[40:41], v[40:41], v[48:49]
	v_pk_mul_f32 v[34:35], v[34:35], v[42:43]
	v_pk_mul_f32 v[36:37], v[36:37], v[44:45]
	s_waitcnt lgkmcnt(0)
	global_store_dwordx4 v[226:227], v[58:61], off
	v_cvt_pk_bf16_f32 v46, v38, v39
	v_cvt_pk_bf16_f32 v47, v40, v41
	v_cvt_pk_bf16_f32 v48, v34, v35
	v_cvt_pk_bf16_f32 v49, v36, v37
	ds_bpermute_b32 v42, v171, v46
	ds_bpermute_b32 v43, v171, v47
	ds_bpermute_b32 v44, v171, v48
	ds_bpermute_b32 v45, v171, v49
	v_add_co_u32_e32 v230, vcc, 0xc6000, v224
	v_addc_co_u32_e32 v231, vcc, 0, v225, vcc
	v_pk_mul_f32 v[30:31], v[30:31], v[218:219] op_sel_hi:[1,0]
	v_pk_mul_f32 v[32:33], v[32:33], v[218:219] op_sel_hi:[1,0]
	v_pk_mul_f32 v[26:27], v[26:27], v[218:219] op_sel_hi:[1,0]
	v_pk_mul_f32 v[28:29], v[28:29], v[218:219] op_sel_hi:[1,0]
	v_exp_f32_e32 v30, v30
	v_exp_f32_e32 v31, v31
	v_exp_f32_e32 v32, v32
	v_exp_f32_e32 v33, v33
	v_exp_f32_e32 v26, v26
	v_exp_f32_e32 v27, v27
	v_exp_f32_e32 v28, v28
	v_exp_f32_e32 v29, v29
	v_pk_fma_f32 v[30:31], v[30:31], v[216:217], v[216:217] op_sel_hi:[1,0,0]
	v_pk_fma_f32 v[32:33], v[32:33], v[216:217], v[216:217] op_sel_hi:[1,0,0]
	v_pk_fma_f32 v[26:27], v[26:27], v[216:217], v[216:217] op_sel_hi:[1,0,0]
	v_pk_fma_f32 v[28:29], v[28:29], v[216:217], v[216:217] op_sel_hi:[1,0,0]
	v_rcp_f32_e32 v30, v30
	v_rcp_f32_e32 v31, v31
	v_rcp_f32_e32 v32, v32
	v_rcp_f32_e32 v33, v33
	v_rcp_f32_e32 v26, v26
	v_rcp_f32_e32 v27, v27
	v_rcp_f32_e32 v28, v28
	v_rcp_f32_e32 v29, v29
	v_pk_mul_f32 v[22:23], v[22:23], v[30:31]
	v_pk_mul_f32 v[24:25], v[24:25], v[32:33]
	v_pk_mul_f32 v[18:19], v[18:19], v[26:27]
	v_pk_mul_f32 v[20:21], v[20:21], v[28:29]
	s_waitcnt lgkmcnt(0)
	global_store_dwordx4 v[230:231], v[42:45], off
	v_cvt_pk_bf16_f32 v30, v22, v23
	v_cvt_pk_bf16_f32 v31, v24, v25
	v_cvt_pk_bf16_f32 v32, v18, v19
	v_cvt_pk_bf16_f32 v33, v20, v21
	ds_bpermute_b32 v26, v171, v30
	ds_bpermute_b32 v27, v171, v31
	ds_bpermute_b32 v28, v171, v32
	ds_bpermute_b32 v29, v171, v33
	v_add_co_u32_e32 v226, vcc, 0xdc000, v224
	v_addc_co_u32_e32 v227, vcc, 0, v225, vcc
	v_pk_mul_f32 v[14:15], v[14:15], v[222:223] op_sel_hi:[1,0]
	v_pk_mul_f32 v[16:17], v[16:17], v[222:223] op_sel_hi:[1,0]
	v_pk_mul_f32 v[10:11], v[10:11], v[222:223] op_sel_hi:[1,0]
	v_pk_mul_f32 v[12:13], v[12:13], v[222:223] op_sel_hi:[1,0]
	v_exp_f32_e32 v14, v14
	v_exp_f32_e32 v15, v15
	v_exp_f32_e32 v16, v16
	v_exp_f32_e32 v17, v17
	v_exp_f32_e32 v10, v10
	v_exp_f32_e32 v11, v11
	v_exp_f32_e32 v12, v12
	v_exp_f32_e32 v13, v13
	v_pk_fma_f32 v[14:15], v[14:15], v[220:221], v[220:221] op_sel_hi:[1,0,0]
	v_pk_fma_f32 v[16:17], v[16:17], v[220:221], v[220:221] op_sel_hi:[1,0,0]
	v_pk_fma_f32 v[10:11], v[10:11], v[220:221], v[220:221] op_sel_hi:[1,0,0]
	v_pk_fma_f32 v[12:13], v[12:13], v[220:221], v[220:221] op_sel_hi:[1,0,0]
	v_rcp_f32_e32 v14, v14
	v_rcp_f32_e32 v15, v15
	v_rcp_f32_e32 v16, v16
	v_rcp_f32_e32 v17, v17
	v_rcp_f32_e32 v10, v10
	v_rcp_f32_e32 v11, v11
	v_rcp_f32_e32 v12, v12
	v_rcp_f32_e32 v13, v13
	v_pk_mul_f32 v[6:7], v[6:7], v[14:15]
	v_pk_mul_f32 v[8:9], v[8:9], v[16:17]
	v_pk_mul_f32 v[2:3], v[2:3], v[10:11]
	v_pk_mul_f32 v[4:5], v[4:5], v[12:13]
	s_waitcnt lgkmcnt(0)
	global_store_dwordx4 v[226:227], v[26:29], off
	v_cvt_pk_bf16_f32 v14, v6, v7
	v_cvt_pk_bf16_f32 v15, v8, v9
	v_cvt_pk_bf16_f32 v16, v2, v3
	v_cvt_pk_bf16_f32 v17, v4, v5
	ds_bpermute_b32 v10, v171, v14
	ds_bpermute_b32 v11, v171, v15
	ds_bpermute_b32 v12, v171, v16
	ds_bpermute_b32 v13, v171, v17
	v_add_co_u32_e32 v230, vcc, 0xf2000, v224
	v_addc_co_u32_e32 v231, vcc, 0, v225, vcc
	s_waitcnt lgkmcnt(0)
	global_store_dwordx4 v[230:231], v[10:13], off
	s_setprio 0
	s_andn2_b64 vcc, exec, s[4:5]
	s_mov_b64 s[20:21], -1
	s_cbranch_vccnz .LBB0_717
	s_andn2_b64 vcc, exec, s[6:7]
	s_cbranch_vccnz .LBB0_716
	s_barrier
	s_branch .LBB0_716

; __device__ __forceinline__ unsigned cvt_pk_bf16(float lo, float hi) { const f32x2c_t v = {lo, hi}; return __builtin_bit_cast(unsigned, __builtin_convertvector(v, bf16x2c_t)); }
; __device__ __forceinline__ void rstd8(const float* SS, int rowb, int lane, float (&rs)[2][4]) {
;     f32x4 p[2][4];
; #pragma unroll
;     for (int ai = 0; ai < 2; ++ai)
; #pragma unroll
;         for (int m = 0; m < 4; ++m) p[ai][m] = *(const f32x4*)(SS + (size_t)(rowb + HALF * ai + 16 * m + (lane >> 2)) * 16 + 4 * (lane & 3));
;     asm volatile("" : "+v"(p[0][0]), "+v"(p[0][1]), "+v"(p[0][2]), "+v"(p[0][3]), "+v"(p[1][0]), "+v"(p[1][1]), "+v"(p[1][2]), "+v"(p[1][3]));
; #pragma unroll
;     for (int ai = 0; ai < 2; ++ai)
; #pragma unroll
;         for (int m = 0; m < 4; ++m) { float s = (p[ai][m][0] + p[ai][m][1]) + (p[ai][m][2] + p[ai][m][3]); s += __shfl_xor(s, 1); s += __shfl_xor(s, 2);
;             const float r = __builtin_amdgcn_rsqf(s * (1.0f / 1024.0f) + RMS_EPS);
;             rs[ai][m] = __builtin_bit_cast(float, __builtin_amdgcn_ds_bpermute((lane & 15) << 4, __builtin_bit_cast(int, r))); }
; }
;     __device__ __forceinline__ void operator()(const f32x4 (&acc)[2][2][4][2], const Unit& u, int wr, int wc, int fr, int fq) const {
;         const int row0 = u.pm * BM + wr * 64 + fr, col0 = u.pn * BM + wc * 32 + 8 * fq;
;         const float sc = (u.pn == 0) ? qs : ((u.pn == 3) ? 0.125f : 1.0f);
;         const int lane = fr + 16 * fq, qs4 = QSRC_ST(lane); const int rowS = u.pm * BM + wr * 64 + (lane >> 2), colS = u.pn * BM + wc * 32 + 8 * (lane & 3);
;         float rs8[2][4]; rstd8(SS, u.pm * BM + wr * 64, lane, rs8);
; #pragma unroll
;         for (int ai = 0; ai < 2; ++ai) {
; #pragma unroll
;             for (int m = 0; m < 4; ++m) { const float rs = rs8[ai][m] * sc;
;                 bf16_t* rowp = U + (size_t)(rowS + ai * HALF + m * 16) * ldu + colS;
; #pragma unroll
;                 for (int bj = 0; bj < 2; ++bj) { const f32x4 v0 = acc[ai][bj][m][0] * rs, v1 = acc[ai][bj][m][1] * rs;
;                     u32x4 w; w.x = cvt_pk_bf16(v0[0], v0[1]); w.y = cvt_pk_bf16(v0[2], v0[3]); w.z = cvt_pk_bf16(v1[0], v1[1]); w.w = cvt_pk_bf16(v1[2], v1[3]);
;                     *(u32x4*)(rowp + bj * HALF) = lane_perm(w, qs4); } } }
.Lepi_prio2:
	s_cmp_eq_u32 s53, 3
	s_cselect_b64 vcc, -1, 0
	v_cndmask_b32_e32 v156, 1.0, v174, vcc
	s_cmp_lg_u32 s53, 0
	s_cselect_b64 vcc, -1, 0
	v_cndmask_b32_e32 v156, v175, v156, vcc
	v_lshl_or_b32 v208, s53, 8, v169
	v_ashrrev_i32_e32 v209, 31, v208
	v_mov_b64_e32 v[154:155], s[44:45]
	v_lshlrev_b64 v[208:209], 1, v[208:209]
	v_mad_i64_i32 v[152:153], s[22:23], v164, s52, v[154:155]
	s_nop 0
	v_lshl_add_u64 v[208:209], v[152:153], 0, v[208:209]
	s_waitcnt vmcnt(0)
	v_add_f32_e32 v176, v176, v177
	v_add_f32_e32 v180, v180, v181
	v_add_f32_e32 v184, v184, v185
	v_add_f32_e32 v188, v188, v189
	v_add_f32_e32 v192, v192, v193
	v_add_f32_e32 v196, v196, v197
	v_add_f32_e32 v200, v200, v201
	v_add_f32_e32 v204, v204, v205
	v_add_f32_e32 v178, v178, v179
	v_add_f32_e32 v182, v182, v183
	v_add_f32_e32 v186, v186, v187
	v_add_f32_e32 v190, v190, v191
	v_add_f32_e32 v194, v194, v195
	v_add_f32_e32 v198, v198, v199
	v_add_f32_e32 v202, v202, v203
	v_add_f32_e32 v206, v206, v207
	v_add_f32_e32 v176, v176, v178
	v_add_f32_e32 v180, v180, v182
	v_add_f32_e32 v184, v184, v186
	v_add_f32_e32 v188, v188, v190
	v_add_f32_e32 v192, v192, v194
	v_add_f32_e32 v196, v196, v198
	v_add_f32_e32 v200, v200, v202
	v_add_f32_e32 v204, v204, v206
	v_add_f32_dpp v176, v176, v176 quad_perm:[1,0,3,2] row_mask:0xf bank_mask:0xf
	v_add_f32_dpp v180, v180, v180 quad_perm:[1,0,3,2] row_mask:0xf bank_mask:0xf
	v_add_f32_dpp v184, v184, v184 quad_perm:[1,0,3,2] row_mask:0xf bank_mask:0xf
	v_add_f32_dpp v188, v188, v188 quad_perm:[1,0,3,2] row_mask:0xf bank_mask:0xf
	v_add_f32_dpp v192, v192, v192 quad_perm:[1,0,3,2] row_mask:0xf bank_mask:0xf
	v_add_f32_dpp v196, v196, v196 quad_perm:[1,0,3,2] row_mask:0xf bank_mask:0xf
	v_add_f32_dpp v200, v200, v200 quad_perm:[1,0,3,2] row_mask:0xf bank_mask:0xf
	v_add_f32_dpp v204, v204, v204 quad_perm:[1,0,3,2] row_mask:0xf bank_mask:0xf
	v_add_f32_dpp v176, v176, v176 quad_perm:[2,3,0,1] row_mask:0xf bank_mask:0xf
	v_add_f32_dpp v180, v180, v180 quad_perm:[2,3,0,1] row_mask:0xf bank_mask:0xf
	v_add_f32_dpp v184, v184, v184 quad_perm:[2,3,0,1] row_mask:0xf bank_mask:0xf
	v_add_f32_dpp v188, v188, v188 quad_perm:[2,3,0,1] row_mask:0xf bank_mask:0xf
	v_add_f32_dpp v192, v192, v192 quad_perm:[2,3,0,1] row_mask:0xf bank_mask:0xf
	v_add_f32_dpp v196, v196, v196 quad_perm:[2,3,0,1] row_mask:0xf bank_mask:0xf
	v_add_f32_dpp v200, v200, v200 quad_perm:[2,3,0,1] row_mask:0xf bank_mask:0xf
	v_add_f32_dpp v204, v204, v204 quad_perm:[2,3,0,1] row_mask:0xf bank_mask:0xf
	v_fmamk_f32 v176, v176, 0x3a800000, v173
	v_fmamk_f32 v180, v180, 0x3a800000, v173
	v_fmamk_f32 v184, v184, 0x3a800000, v173
	v_fmamk_f32 v188, v188, 0x3a800000, v173
	v_fmamk_f32 v192, v192, 0x3a800000, v173
	v_fmamk_f32 v196, v196, 0x3a800000, v173
	v_fmamk_f32 v200, v200, 0x3a800000, v173
	v_fmamk_f32 v204, v204, 0x3a800000, v173
	ds_bpermute_b32 v176, v168, v176
	ds_bpermute_b32 v180, v168, v180
	ds_bpermute_b32 v184, v168, v184
	ds_bpermute_b32 v188, v168, v188
	ds_bpermute_b32 v192, v168, v192
	ds_bpermute_b32 v196, v168, v196
	ds_bpermute_b32 v200, v168, v200
	ds_bpermute_b32 v204, v168, v204
	s_waitcnt lgkmcnt(0)
	v_rsq_f32_e32 v178, v176
	v_rsq_f32_e32 v182, v180
	v_rsq_f32_e32 v186, v184
	v_rsq_f32_e32 v190, v188
	v_rsq_f32_e32 v194, v192
	v_rsq_f32_e32 v198, v196
	v_rsq_f32_e32 v202, v200
	v_rsq_f32_e32 v206, v204
	v_mul_f32_e32 v178, v156, v178
	v_mul_f32_e32 v182, v156, v182
	v_mul_f32_e32 v186, v156, v186
	v_mul_f32_e32 v190, v156, v190
	v_mul_f32_e32 v194, v156, v194
	v_mul_f32_e32 v198, v156, v198
	v_mul_f32_e32 v202, v156, v202
	v_mul_f32_e32 v206, v156, v206
	v_pk_mul_f32 v[126:127], v[126:127], v[178:179] op_sel_hi:[1,0]
	v_pk_mul_f32 v[128:129], v[128:129], v[178:179] op_sel_hi:[1,0]
	v_pk_mul_f32 v[122:123], v[122:123], v[178:179] op_sel_hi:[1,0]
	v_pk_mul_f32 v[124:125], v[124:125], v[178:179] op_sel_hi:[1,0]
	v_pk_mul_f32 v[118:119], v[118:119], v[178:179] op_sel_hi:[1,0]
	v_pk_mul_f32 v[120:121], v[120:121], v[178:179] op_sel_hi:[1,0]
	v_pk_mul_f32 v[110:111], v[110:111], v[178:179] op_sel_hi:[1,0]
	v_pk_mul_f32 v[112:113], v[112:113], v[178:179] op_sel_hi:[1,0]
	v_cvt_pk_bf16_f32 v126, v126, v127
	v_cvt_pk_bf16_f32 v127, v128, v129
	v_cvt_pk_bf16_f32 v128, v122, v123
	v_cvt_pk_bf16_f32 v129, v124, v125
	v_cvt_pk_bf16_f32 v118, v118, v119
	v_cvt_pk_bf16_f32 v119, v120, v121
	v_cvt_pk_bf16_f32 v120, v110, v111
	v_cvt_pk_bf16_f32 v121, v112, v113
	ds_bpermute_b32 v122, v166, v126
	ds_bpermute_b32 v123, v166, v127
	ds_bpermute_b32 v124, v166, v128
	ds_bpermute_b32 v125, v166, v129
	ds_bpermute_b32 v110, v166, v118
	ds_bpermute_b32 v111, v166, v119
	ds_bpermute_b32 v112, v166, v120
	ds_bpermute_b32 v113, v166, v121
	v_mov_b32_e32 v210, v208
	v_mov_b32_e32 v211, v209
	v_pk_mul_f32 v[114:115], v[114:115], v[182:183] op_sel_hi:[1,0]
	v_pk_mul_f32 v[116:117], v[116:117], v[182:183] op_sel_hi:[1,0]
	v_pk_mul_f32 v[106:107], v[106:107], v[182:183] op_sel_hi:[1,0]
	v_pk_mul_f32 v[108:109], v[108:109], v[182:183] op_sel_hi:[1,0]
	v_pk_mul_f32 v[102:103], v[102:103], v[182:183] op_sel_hi:[1,0]
	v_pk_mul_f32 v[104:105], v[104:105], v[182:183] op_sel_hi:[1,0]
	v_pk_mul_f32 v[94:95], v[94:95], v[182:183] op_sel_hi:[1,0]
	v_pk_mul_f32 v[96:97], v[96:97], v[182:183] op_sel_hi:[1,0]
	v_cvt_pk_bf16_f32 v114, v114, v115
	v_cvt_pk_bf16_f32 v115, v116, v117
	v_cvt_pk_bf16_f32 v116, v106, v107
	v_cvt_pk_bf16_f32 v117, v108, v109
	v_cvt_pk_bf16_f32 v102, v102, v103
	v_cvt_pk_bf16_f32 v103, v104, v105
	v_cvt_pk_bf16_f32 v104, v94, v95
	v_cvt_pk_bf16_f32 v105, v96, v97
	ds_bpermute_b32 v106, v166, v114
	ds_bpermute_b32 v107, v166, v115
	ds_bpermute_b32 v108, v166, v116
	ds_bpermute_b32 v109, v166, v117
	ds_bpermute_b32 v94, v166, v102
	ds_bpermute_b32 v95, v166, v103
	ds_bpermute_b32 v96, v166, v104
	ds_bpermute_b32 v97, v166, v105
	v_add_co_u32_e32 v212, vcc, 0x18000, v208
	v_addc_co_u32_e32 v213, vcc, 0, v209, vcc
	s_waitcnt lgkmcnt(8)
; __device__ __forceinline__ unsigned cvt_pk_bf16(float lo, float hi) { const f32x2c_t v = {lo, hi}; return __builtin_bit_cast(unsigned, __builtin_convertvector(v, bf16x2c_t)); }
;     __device__ __forceinline__ void operator()(const f32x4 (&acc)[2][2][4][2], const Unit& u, int wr, int wc, int fr, int fq) const {
;     ...
;             for (int m = 0; m < 4; ++m) { const float rs = rs8[ai][m] * sc;
;                 bf16_t* rowp = U + (size_t)(rowS + ai * HALF + m * 16) * ldu + colS;
; #pragma unroll
;                 for (int bj = 0; bj < 2; ++bj) { const f32x4 v0 = acc[ai][bj][m][0] * rs, v1 = acc[ai][bj][m][1] * rs;
;                     u32x4 w; w.x = cvt_pk_bf16(v0[0], v0[1]); w.y = cvt_pk_bf16(v0[2], v0[3]); w.z = cvt_pk_bf16(v1[0], v1[1]); w.w = cvt_pk_bf16(v1[2], v1[3]);
;                     *(u32x4*)(rowp + bj * HALF) = lane_perm(w, qs4); } } }
	global_store_dwordx4 v[210:211], v[122:125], off
	global_store_dwordx4 v[210:211], v[110:113], off offset:256
	v_pk_mul_f32 v[98:99], v[98:99], v[186:187] op_sel_hi:[1,0]
	v_pk_mul_f32 v[100:101], v[100:101], v[186:187] op_sel_hi:[1,0]
	v_pk_mul_f32 v[90:91], v[90:91], v[186:187] op_sel_hi:[1,0]
	v_pk_mul_f32 v[92:93], v[92:93], v[186:187] op_sel_hi:[1,0]
	v_pk_mul_f32 v[86:87], v[86:87], v[186:187] op_sel_hi:[1,0]
	v_pk_mul_f32 v[88:89], v[88:89], v[186:187] op_sel_hi:[1,0]
	v_pk_mul_f32 v[78:79], v[78:79], v[186:187] op_sel_hi:[1,0]
	v_pk_mul_f32 v[80:81], v[80:81], v[186:187] op_sel_hi:[1,0]
	v_cvt_pk_bf16_f32 v98, v98, v99
	v_cvt_pk_bf16_f32 v99, v100, v101
	v_cvt_pk_bf16_f32 v100, v90, v91
	v_cvt_pk_bf16_f32 v101, v92, v93
	v_cvt_pk_bf16_f32 v86, v86, v87
	v_cvt_pk_bf16_f32 v87, v88, v89
	v_cvt_pk_bf16_f32 v88, v78, v79
	v_cvt_pk_bf16_f32 v89, v80, v81
	ds_bpermute_b32 v90, v166, v98
	ds_bpermute_b32 v91, v166, v99
	ds_bpermute_b32 v92, v166, v100
	ds_bpermute_b32 v93, v166, v101
	ds_bpermute_b32 v78, v166, v86
	ds_bpermute_b32 v79, v166, v87
	ds_bpermute_b32 v80, v166, v88
	ds_bpermute_b32 v81, v166, v89
	v_add_co_u32_e32 v210, vcc, 0x30000, v208
	v_addc_co_u32_e32 v211, vcc, 0, v209, vcc
	s_waitcnt lgkmcnt(8)
	global_store_dwordx4 v[212:213], v[106:109], off
	global_store_dwordx4 v[212:213], v[94:97], off offset:256
	v_pk_mul_f32 v[82:83], v[82:83], v[190:191] op_sel_hi:[1,0]
	v_pk_mul_f32 v[84:85], v[84:85], v[190:191] op_sel_hi:[1,0]
	v_pk_mul_f32 v[74:75], v[74:75], v[190:191] op_sel_hi:[1,0]
	v_pk_mul_f32 v[76:77], v[76:77], v[190:191] op_sel_hi:[1,0]
	v_pk_mul_f32 v[70:71], v[70:71], v[190:191] op_sel_hi:[1,0]
	v_pk_mul_f32 v[72:73], v[72:73], v[190:191] op_sel_hi:[1,0]
	v_pk_mul_f32 v[66:67], v[66:67], v[190:191] op_sel_hi:[1,0]
	v_pk_mul_f32 v[68:69], v[68:69], v[190:191] op_sel_hi:[1,0]
	v_cvt_pk_bf16_f32 v82, v82, v83
	v_cvt_pk_bf16_f32 v83, v84, v85
	v_cvt_pk_bf16_f32 v84, v74, v75
	v_cvt_pk_bf16_f32 v85, v76, v77
	v_cvt_pk_bf16_f32 v70, v70, v71
	v_cvt_pk_bf16_f32 v71, v72, v73
	v_cvt_pk_bf16_f32 v72, v66, v67
	v_cvt_pk_bf16_f32 v73, v68, v69
	ds_bpermute_b32 v74, v166, v82
	ds_bpermute_b32 v75, v166, v83
	ds_bpermute_b32 v76, v166, v84
	ds_bpermute_b32 v77, v166, v85
	ds_bpermute_b32 v66, v166, v70
	ds_bpermute_b32 v67, v166, v71
	ds_bpermute_b32 v68, v166, v72
	ds_bpermute_b32 v69, v166, v73
	v_add_co_u32_e32 v212, vcc, 0x48000, v208
	v_addc_co_u32_e32 v213, vcc, 0, v209, vcc
	s_waitcnt lgkmcnt(8)
	global_store_dwordx4 v[210:211], v[90:93], off
	global_store_dwordx4 v[210:211], v[78:81], off offset:256
	v_pk_mul_f32 v[62:63], v[62:63], v[194:195] op_sel_hi:[1,0]
	v_pk_mul_f32 v[64:65], v[64:65], v[194:195] op_sel_hi:[1,0]
	v_pk_mul_f32 v[58:59], v[58:59], v[194:195] op_sel_hi:[1,0]
	v_pk_mul_f32 v[60:61], v[60:61], v[194:195] op_sel_hi:[1,0]
	v_pk_mul_f32 v[54:55], v[54:55], v[194:195] op_sel_hi:[1,0]
	v_pk_mul_f32 v[56:57], v[56:57], v[194:195] op_sel_hi:[1,0]
	v_pk_mul_f32 v[46:47], v[46:47], v[194:195] op_sel_hi:[1,0]
	v_pk_mul_f32 v[48:49], v[48:49], v[194:195] op_sel_hi:[1,0]
	v_cvt_pk_bf16_f32 v62, v62, v63
	v_cvt_pk_bf16_f32 v63, v64, v65
	v_cvt_pk_bf16_f32 v64, v58, v59
	v_cvt_pk_bf16_f32 v65, v60, v61
	v_cvt_pk_bf16_f32 v54, v54, v55
	v_cvt_pk_bf16_f32 v55, v56, v57
	v_cvt_pk_bf16_f32 v56, v46, v47
	v_cvt_pk_bf16_f32 v57, v48, v49
	ds_bpermute_b32 v58, v166, v62
	ds_bpermute_b32 v59, v166, v63
	ds_bpermute_b32 v60, v166, v64
	ds_bpermute_b32 v61, v166, v65
	ds_bpermute_b32 v46, v166, v54
	ds_bpermute_b32 v47, v166, v55
	ds_bpermute_b32 v48, v166, v56
	ds_bpermute_b32 v49, v166, v57
	v_add_co_u32_e32 v210, vcc, 0xc0000, v208
	v_addc_co_u32_e32 v211, vcc, 0, v209, vcc
	s_waitcnt lgkmcnt(8)
; __device__ __forceinline__ unsigned cvt_pk_bf16(float lo, float hi) { const f32x2c_t v = {lo, hi}; return __builtin_bit_cast(unsigned, __builtin_convertvector(v, bf16x2c_t)); }
; #define PG8_BAR __builtin_amdgcn_s_barrier()
;     __device__ __forceinline__ void operator()(const f32x4 (&acc)[2][2][4][2], const Unit& u, int wr, int wc, int fr, int fq) const {
;     ...
;             for (int m = 0; m < 4; ++m) { const float rs = rs8[ai][m] * sc;
;                 bf16_t* rowp = U + (size_t)(rowS + ai * HALF + m * 16) * ldu + colS;
; #pragma unroll
;                 for (int bj = 0; bj < 2; ++bj) { const f32x4 v0 = acc[ai][bj][m][0] * rs, v1 = acc[ai][bj][m][1] * rs;
;                     u32x4 w; w.x = cvt_pk_bf16(v0[0], v0[1]); w.y = cvt_pk_bf16(v0[2], v0[3]); w.z = cvt_pk_bf16(v1[0], v1[1]); w.w = cvt_pk_bf16(v1[2], v1[3]);
;                     *(u32x4*)(rowp + bj * HALF) = lane_perm(w, qs4); } } }
; template <class Epi, class Sched, bool ALIGN_EPI = false, bool SP2 = false>
; __device__ __forceinline__ void gemm_phase(PG8_LAS unsigned char* lds, const Gemm g, const Sched& S, const Epi& E, const bool skip_epi = false) {
;     ...
;         if constexpr (!Epi::AFTER_DRAIN) { if (!skip_epi) E(acc, cur, wr, wc, fr, fq); S.done(cur); }
;         if (!has_next) break;
; #pragma unroll
;         for (int a = 0; a < 2; ++a)
; #pragma unroll
;             for (int b = 0; b < 2; ++b)
; #pragma unroll
;                 for (int m = 0; m < 4; ++m)
; #pragma unroll
;                     for (int n = 0; n < 2; ++n) acc[a][b][m][n] = (f32x4){0.f, 0.f, 0.f, 0.f};
;         cur = nxt; cA = nA; cB = nB; ++ui;
;         if constexpr (Sched::GATHER) { gA[0][0] = gN[0][0]; gA[0][1] = gN[0][1]; gA[1][0] = gN[1][0]; gA[1][1] = gN[1][1]; }
;         if constexpr (ALIGN_EPI) { if (wr == 1) PG8_BAR; }
	global_store_dwordx4 v[212:213], v[74:77], off
	global_store_dwordx4 v[212:213], v[66:69], off offset:256
	v_pk_mul_f32 v[50:51], v[50:51], v[198:199] op_sel_hi:[1,0]
	v_pk_mul_f32 v[52:53], v[52:53], v[198:199] op_sel_hi:[1,0]
	v_pk_mul_f32 v[42:43], v[42:43], v[198:199] op_sel_hi:[1,0]
	v_pk_mul_f32 v[44:45], v[44:45], v[198:199] op_sel_hi:[1,0]
	v_pk_mul_f32 v[38:39], v[38:39], v[198:199] op_sel_hi:[1,0]
	v_pk_mul_f32 v[40:41], v[40:41], v[198:199] op_sel_hi:[1,0]
	v_pk_mul_f32 v[30:31], v[30:31], v[198:199] op_sel_hi:[1,0]
	v_pk_mul_f32 v[32:33], v[32:33], v[198:199] op_sel_hi:[1,0]
	v_cvt_pk_bf16_f32 v50, v50, v51
	v_cvt_pk_bf16_f32 v51, v52, v53
	v_cvt_pk_bf16_f32 v52, v42, v43
	v_cvt_pk_bf16_f32 v53, v44, v45
	v_cvt_pk_bf16_f32 v38, v38, v39
	v_cvt_pk_bf16_f32 v39, v40, v41
	v_cvt_pk_bf16_f32 v40, v30, v31
	v_cvt_pk_bf16_f32 v41, v32, v33
	ds_bpermute_b32 v42, v166, v50
	ds_bpermute_b32 v43, v166, v51
	ds_bpermute_b32 v44, v166, v52
	ds_bpermute_b32 v45, v166, v53
	ds_bpermute_b32 v30, v166, v38
	ds_bpermute_b32 v31, v166, v39
	ds_bpermute_b32 v32, v166, v40
	ds_bpermute_b32 v33, v166, v41
	v_add_co_u32_e32 v212, vcc, 0xd8000, v208
	v_addc_co_u32_e32 v213, vcc, 0, v209, vcc
	s_waitcnt lgkmcnt(8)
	global_store_dwordx4 v[210:211], v[58:61], off
	global_store_dwordx4 v[210:211], v[46:49], off offset:256
	v_pk_mul_f32 v[34:35], v[34:35], v[202:203] op_sel_hi:[1,0]
	v_pk_mul_f32 v[36:37], v[36:37], v[202:203] op_sel_hi:[1,0]
	v_pk_mul_f32 v[26:27], v[26:27], v[202:203] op_sel_hi:[1,0]
	v_pk_mul_f32 v[28:29], v[28:29], v[202:203] op_sel_hi:[1,0]
	v_pk_mul_f32 v[22:23], v[22:23], v[202:203] op_sel_hi:[1,0]
	v_pk_mul_f32 v[24:25], v[24:25], v[202:203] op_sel_hi:[1,0]
	v_pk_mul_f32 v[14:15], v[14:15], v[202:203] op_sel_hi:[1,0]
	v_pk_mul_f32 v[16:17], v[16:17], v[202:203] op_sel_hi:[1,0]
	v_cvt_pk_bf16_f32 v34, v34, v35
	v_cvt_pk_bf16_f32 v35, v36, v37
	v_cvt_pk_bf16_f32 v36, v26, v27
	v_cvt_pk_bf16_f32 v37, v28, v29
	v_cvt_pk_bf16_f32 v22, v22, v23
	v_cvt_pk_bf16_f32 v23, v24, v25
	v_cvt_pk_bf16_f32 v24, v14, v15
	v_cvt_pk_bf16_f32 v25, v16, v17
	ds_bpermute_b32 v26, v166, v34
	ds_bpermute_b32 v27, v166, v35
	ds_bpermute_b32 v28, v166, v36
	ds_bpermute_b32 v29, v166, v37
	ds_bpermute_b32 v14, v166, v22
	ds_bpermute_b32 v15, v166, v23
	ds_bpermute_b32 v16, v166, v24
	ds_bpermute_b32 v17, v166, v25
	v_add_co_u32_e32 v210, vcc, 0xf0000, v208
	v_addc_co_u32_e32 v211, vcc, 0, v209, vcc
	s_waitcnt lgkmcnt(8)
	global_store_dwordx4 v[212:213], v[42:45], off
	global_store_dwordx4 v[212:213], v[30:33], off offset:256
	v_pk_mul_f32 v[18:19], v[18:19], v[206:207] op_sel_hi:[1,0]
	v_pk_mul_f32 v[20:21], v[20:21], v[206:207] op_sel_hi:[1,0]
	v_pk_mul_f32 v[10:11], v[10:11], v[206:207] op_sel_hi:[1,0]
	v_pk_mul_f32 v[12:13], v[12:13], v[206:207] op_sel_hi:[1,0]
	v_pk_mul_f32 v[6:7], v[6:7], v[206:207] op_sel_hi:[1,0]
	v_pk_mul_f32 v[8:9], v[8:9], v[206:207] op_sel_hi:[1,0]
	v_pk_mul_f32 v[2:3], v[2:3], v[206:207] op_sel_hi:[1,0]
	v_pk_mul_f32 v[4:5], v[4:5], v[206:207] op_sel_hi:[1,0]
	v_cvt_pk_bf16_f32 v18, v18, v19
	v_cvt_pk_bf16_f32 v19, v20, v21
	v_cvt_pk_bf16_f32 v20, v10, v11
	v_cvt_pk_bf16_f32 v21, v12, v13
	v_cvt_pk_bf16_f32 v6, v6, v7
	v_cvt_pk_bf16_f32 v7, v8, v9
	v_cvt_pk_bf16_f32 v8, v2, v3
	v_cvt_pk_bf16_f32 v9, v4, v5
	ds_bpermute_b32 v10, v166, v18
	ds_bpermute_b32 v11, v166, v19
	ds_bpermute_b32 v12, v166, v20
	ds_bpermute_b32 v13, v166, v21
	ds_bpermute_b32 v2, v166, v6
	ds_bpermute_b32 v3, v166, v7
	ds_bpermute_b32 v4, v166, v8
	ds_bpermute_b32 v5, v166, v9
	v_add_co_u32_e32 v212, vcc, 0x108000, v208
	v_addc_co_u32_e32 v213, vcc, 0, v209, vcc
	s_waitcnt lgkmcnt(8)
	global_store_dwordx4 v[210:211], v[26:29], off
	global_store_dwordx4 v[210:211], v[14:17], off offset:256
	s_waitcnt lgkmcnt(0)
	global_store_dwordx4 v[212:213], v[10:13], off
	global_store_dwordx4 v[212:213], v[2:5], off offset:256
	s_setprio 0
	s_andn2_b64 vcc, exec, s[4:5]
	s_mov_b64 s[4:5], -1
	s_cbranch_vccnz .LBB0_940
	s_andn2_b64 vcc, exec, s[6:7]
	s_cbranch_vccnz .LBB0_939
	s_barrier
	s_branch .LBB0_939

; __device__ __forceinline__ unsigned cvt_pk_bf16(float lo, float hi) { const f32x2c_t v = {lo, hi}; return __builtin_bit_cast(unsigned, __builtin_convertvector(v, bf16x2c_t)); }
; __device__ __forceinline__ float silu_f(float a) { return a * __builtin_amdgcn_rcpf(1.0f + __builtin_amdgcn_exp2f(a * -1.4426950408889634f)); }
;     __device__ __forceinline__ void operator()(const f32x4 (&acc)[2][2][4][2], const Unit& u, int wr, int wc, int fr, int fq) const {
;         const int row0 = u.pm * BM + wr * 64 + fr; const int pnl = MOE ? (u.pn % 28) : u.pn;
;         const int lane = fr + 16 * fq, qs4 = QSRC_ST(lane); const int rowS = u.pm * BM + wr * 64 + (lane >> 2), colS = pnl * HALF + wc * 32 + 8 * (lane & 3);
;         float rs8[2][4];
;         if constexpr (MOE) {
; #pragma unroll
;             for (int ai = 0; ai < 2; ++ai)
; #pragma unroll
;                 for (int m = 0; m < 4; ++m) rs8[ai][m] = SS[row0 + ai * HALF + m * 16];
;             asm volatile("" : "+v"(rs8[0][0]), "+v"(rs8[0][1]), "+v"(rs8[0][2]), "+v"(rs8[0][3]), "+v"(rs8[1][0]), "+v"(rs8[1][1]), "+v"(rs8[1][2]), "+v"(rs8[1][3]));
;         } else rstd8(SS, u.pm * BM + wr * 64, lane, rs8);
; #pragma unroll
;         for (int ai = 0; ai < 2; ++ai) {
; #pragma unroll
;             for (int m = 0; m < 4; ++m) { const int row = row0 + ai * HALF + m * 16; const float rs = rs8[ai][m];
;                 const f32x4 a0 = acc[ai][0][m][0] * rs, a1 = acc[ai][0][m][1] * rs, b0 = acc[ai][1][m][0] * rs, b1 = acc[ai][1][m][1] * rs;
;                 f32x4 g0, g1;
; #pragma unroll
;                 for (int j = 0; j < 4; ++j) { g0[j] = silu_f(a0[j]) * b0[j]; g1[j] = silu_f(a1[j]) * b1[j]; }
;                 u32x4 w; w.x = cvt_pk_bf16(g0[0], g0[1]); w.y = cvt_pk_bf16(g0[2], g0[3]); w.z = cvt_pk_bf16(g1[0], g1[1]); w.w = cvt_pk_bf16(g1[2], g1[3]);
;                 w = lane_perm(w, qs4); u32x4* dst = (u32x4*)(O + (size_t)(rowS + ai * HALF + m * 16) * ldo + colS); (void)row;
;                 if constexpr (MOE) __builtin_nontemporal_store(w, dst); else *dst = w; } }
.LBB0_1731:
	s_and_b64 vcc, exec, s[26:27]
	s_cbranch_vccz .Lepi_prio3
	s_setprio 2
.Lepi_prio3:
	s_lshl_b32 s6, s38, 8
	s_add_i32 s6, s6, s54
	s_mul_hi_i32 s7, s36, 0x92492493
	v_readlane_b32 s40, v254, 36
	s_add_i32 s7, s7, s36
	v_readlane_b32 s41, v254, 37
	v_or_b32_e32 v147, s6, v155
	s_lshr_b32 s6, s7, 31
	s_lshr_b32 s7, s7, 4
	v_mov_b64_e32 v[140:141], s[40:41]
	s_add_i32 s29, s7, s6
	v_mad_i64_i32 v[170:171], s[6:7], v147, s60, v[140:141]
	s_mul_i32 s29, s29, 28
	s_sub_i32 s6, s36, s29
	v_lshl_or_b32 v142, s6, 7, v157
	v_ashrrev_i32_e32 v143, 31, v142
	v_lshlrev_b64 v[142:143], 1, v[142:143]
	v_lshl_add_u64 v[170:171], v[170:171], 0, v[142:143]
	v_mul_f32_e32 v248, 0xbfb8aa3b, v247
	v_mul_f32_e32 v250, v247, v247
	v_rcp_f32_e32 v250, v250
	v_pk_mul_f32 v[118:119], v[118:119], v[126:127]
	v_pk_mul_f32 v[120:121], v[120:121], v[128:129]
	v_pk_mul_f32 v[114:115], v[114:115], v[122:123]
	v_pk_mul_f32 v[116:117], v[116:117], v[124:125]
	v_pk_mul_f32 v[126:127], v[126:127], v[248:249] op_sel_hi:[1,0]
	v_pk_mul_f32 v[128:129], v[128:129], v[248:249] op_sel_hi:[1,0]
	v_pk_mul_f32 v[122:123], v[122:123], v[248:249] op_sel_hi:[1,0]
	v_pk_mul_f32 v[124:125], v[124:125], v[248:249] op_sel_hi:[1,0]
	v_exp_f32_e32 v126, v126
	v_exp_f32_e32 v127, v127
	v_exp_f32_e32 v128, v128
	v_exp_f32_e32 v129, v129
	v_exp_f32_e32 v122, v122
	v_exp_f32_e32 v123, v123
	v_exp_f32_e32 v124, v124
	v_exp_f32_e32 v125, v125
	v_pk_fma_f32 v[126:127], v[126:127], v[250:251], v[250:251] op_sel_hi:[1,0,0]
	v_pk_fma_f32 v[128:129], v[128:129], v[250:251], v[250:251] op_sel_hi:[1,0,0]
	v_pk_fma_f32 v[122:123], v[122:123], v[250:251], v[250:251] op_sel_hi:[1,0,0]
	v_pk_fma_f32 v[124:125], v[124:125], v[250:251], v[250:251] op_sel_hi:[1,0,0]
	v_rcp_f32_e32 v126, v126
	v_rcp_f32_e32 v127, v127
	v_rcp_f32_e32 v128, v128
	v_rcp_f32_e32 v129, v129
	v_rcp_f32_e32 v122, v122
	v_rcp_f32_e32 v123, v123
	v_rcp_f32_e32 v124, v124
	v_rcp_f32_e32 v125, v125
	v_pk_mul_f32 v[118:119], v[118:119], v[126:127]
	v_pk_mul_f32 v[120:121], v[120:121], v[128:129]
	v_pk_mul_f32 v[114:115], v[114:115], v[122:123]
	v_pk_mul_f32 v[116:117], v[116:117], v[124:125]
	v_cvt_pk_bf16_f32 v126, v118, v119
	v_cvt_pk_bf16_f32 v127, v120, v121
	v_cvt_pk_bf16_f32 v128, v114, v115
	v_cvt_pk_bf16_f32 v129, v116, v117
	ds_bpermute_b32 v122, v156, v126
	ds_bpermute_b32 v123, v156, v127
	ds_bpermute_b32 v124, v156, v128
	ds_bpermute_b32 v125, v156, v129
	v_mov_b32_e32 v140, v170
	v_mov_b32_e32 v141, v171
	v_mul_f32_e32 v248, 0xbfb8aa3b, v246
	v_mul_f32_e32 v250, v246, v246
	v_rcp_f32_e32 v250, v250
	v_pk_mul_f32 v[102:103], v[102:103], v[110:111]
	v_pk_mul_f32 v[104:105], v[104:105], v[112:113]
	v_pk_mul_f32 v[98:99], v[98:99], v[106:107]
	v_pk_mul_f32 v[100:101], v[100:101], v[108:109]
	v_pk_mul_f32 v[110:111], v[110:111], v[248:249] op_sel_hi:[1,0]
	v_pk_mul_f32 v[112:113], v[112:113], v[248:249] op_sel_hi:[1,0]
	v_pk_mul_f32 v[106:107], v[106:107], v[248:249] op_sel_hi:[1,0]
	v_pk_mul_f32 v[108:109], v[108:109], v[248:249] op_sel_hi:[1,0]
	v_exp_f32_e32 v110, v110
	v_exp_f32_e32 v111, v111
	v_exp_f32_e32 v112, v112
	v_exp_f32_e32 v113, v113
	v_exp_f32_e32 v106, v106
	v_exp_f32_e32 v107, v107
	v_exp_f32_e32 v108, v108
	v_exp_f32_e32 v109, v109
	v_pk_fma_f32 v[110:111], v[110:111], v[250:251], v[250:251] op_sel_hi:[1,0,0]
	v_pk_fma_f32 v[112:113], v[112:113], v[250:251], v[250:251] op_sel_hi:[1,0,0]
	v_pk_fma_f32 v[106:107], v[106:107], v[250:251], v[250:251] op_sel_hi:[1,0,0]
	v_pk_fma_f32 v[108:109], v[108:109], v[250:251], v[250:251] op_sel_hi:[1,0,0]
	v_rcp_f32_e32 v110, v110
	v_rcp_f32_e32 v111, v111
	v_rcp_f32_e32 v112, v112
	v_rcp_f32_e32 v113, v113
	v_rcp_f32_e32 v106, v106
	v_rcp_f32_e32 v107, v107
	v_rcp_f32_e32 v108, v108
	v_rcp_f32_e32 v109, v109
	v_pk_mul_f32 v[102:103], v[102:103], v[110:111]
	v_pk_mul_f32 v[104:105], v[104:105], v[112:113]
	v_pk_mul_f32 v[98:99], v[98:99], v[106:107]
	v_pk_mul_f32 v[100:101], v[100:101], v[108:109]
	s_waitcnt lgkmcnt(0)
	global_store_dwordx4 v[140:141], v[122:125], off nt
	v_cvt_pk_bf16_f32 v110, v102, v103
	v_cvt_pk_bf16_f32 v111, v104, v105
	v_cvt_pk_bf16_f32 v112, v98, v99
	v_cvt_pk_bf16_f32 v113, v100, v101
	ds_bpermute_b32 v106, v156, v110
	ds_bpermute_b32 v107, v156, v111
	ds_bpermute_b32 v108, v156, v112
	ds_bpermute_b32 v109, v156, v113
	v_add_co_u32_e32 v142, vcc, 0x1c000, v170
	v_addc_co_u32_e32 v143, vcc, 0, v171, vcc
	v_mul_f32_e32 v248, 0xbfb8aa3b, v245
	v_mul_f32_e32 v250, v245, v245
	v_rcp_f32_e32 v250, v250
	v_pk_mul_f32 v[86:87], v[86:87], v[94:95]
	v_pk_mul_f32 v[88:89], v[88:89], v[96:97]
	v_pk_mul_f32 v[82:83], v[82:83], v[90:91]
	v_pk_mul_f32 v[84:85], v[84:85], v[92:93]
	v_pk_mul_f32 v[94:95], v[94:95], v[248:249] op_sel_hi:[1,0]
	v_pk_mul_f32 v[96:97], v[96:97], v[248:249] op_sel_hi:[1,0]
	v_pk_mul_f32 v[90:91], v[90:91], v[248:249] op_sel_hi:[1,0]
	v_pk_mul_f32 v[92:93], v[92:93], v[248:249] op_sel_hi:[1,0]
	v_exp_f32_e32 v94, v94
	v_exp_f32_e32 v95, v95
	v_exp_f32_e32 v96, v96
	v_exp_f32_e32 v97, v97
	v_exp_f32_e32 v90, v90
	v_exp_f32_e32 v91, v91
	v_exp_f32_e32 v92, v92
	v_exp_f32_e32 v93, v93
	v_pk_fma_f32 v[94:95], v[94:95], v[250:251], v[250:251] op_sel_hi:[1,0,0]
	v_pk_fma_f32 v[96:97], v[96:97], v[250:251], v[250:251] op_sel_hi:[1,0,0]
	v_pk_fma_f32 v[90:91], v[90:91], v[250:251], v[250:251] op_sel_hi:[1,0,0]
	v_pk_fma_f32 v[92:93], v[92:93], v[250:251], v[250:251] op_sel_hi:[1,0,0]
	v_rcp_f32_e32 v94, v94
	v_rcp_f32_e32 v95, v95
	v_rcp_f32_e32 v96, v96
	v_rcp_f32_e32 v97, v97
	v_rcp_f32_e32 v90, v90
	v_rcp_f32_e32 v91, v91
	v_rcp_f32_e32 v92, v92
	v_rcp_f32_e32 v93, v93
	v_pk_mul_f32 v[86:87], v[86:87], v[94:95]
	v_pk_mul_f32 v[88:89], v[88:89], v[96:97]
	v_pk_mul_f32 v[82:83], v[82:83], v[90:91]
	v_pk_mul_f32 v[84:85], v[84:85], v[92:93]
	s_waitcnt lgkmcnt(0)
; __device__ __forceinline__ unsigned cvt_pk_bf16(float lo, float hi) { const f32x2c_t v = {lo, hi}; return __builtin_bit_cast(unsigned, __builtin_convertvector(v, bf16x2c_t)); }
; __device__ __forceinline__ float silu_f(float a) { return a * __builtin_amdgcn_rcpf(1.0f + __builtin_amdgcn_exp2f(a * -1.4426950408889634f)); }
;     __device__ __forceinline__ void operator()(const f32x4 (&acc)[2][2][4][2], const Unit& u, int wr, int wc, int fr, int fq) const {
;     ...
;         for (int ai = 0; ai < 2; ++ai) {
; #pragma unroll
;             for (int m = 0; m < 4; ++m) { const int row = row0 + ai * HALF + m * 16; const float rs = rs8[ai][m];
;                 const f32x4 a0 = acc[ai][0][m][0] * rs, a1 = acc[ai][0][m][1] * rs, b0 = acc[ai][1][m][0] * rs, b1 = acc[ai][1][m][1] * rs;
;                 f32x4 g0, g1;
; #pragma unroll
;                 for (int j = 0; j < 4; ++j) { g0[j] = silu_f(a0[j]) * b0[j]; g1[j] = silu_f(a1[j]) * b1[j]; }
;                 u32x4 w; w.x = cvt_pk_bf16(g0[0], g0[1]); w.y = cvt_pk_bf16(g0[2], g0[3]); w.z = cvt_pk_bf16(g1[0], g1[1]); w.w = cvt_pk_bf16(g1[2], g1[3]);
;                 w = lane_perm(w, qs4); u32x4* dst = (u32x4*)(O + (size_t)(rowS + ai * HALF + m * 16) * ldo + colS); (void)row;
;                 if constexpr (MOE) __builtin_nontemporal_store(w, dst); else *dst = w; } }
	global_store_dwordx4 v[142:143], v[106:109], off nt
	v_cvt_pk_bf16_f32 v94, v86, v87
	v_cvt_pk_bf16_f32 v95, v88, v89
	v_cvt_pk_bf16_f32 v96, v82, v83
	v_cvt_pk_bf16_f32 v97, v84, v85
	ds_bpermute_b32 v90, v156, v94
	ds_bpermute_b32 v91, v156, v95
	ds_bpermute_b32 v92, v156, v96
	ds_bpermute_b32 v93, v156, v97
	v_add_co_u32_e32 v140, vcc, 0x38000, v170
	v_addc_co_u32_e32 v141, vcc, 0, v171, vcc
	v_mul_f32_e32 v248, 0xbfb8aa3b, v244
	v_mul_f32_e32 v250, v244, v244
	v_rcp_f32_e32 v250, v250
	v_pk_mul_f32 v[70:71], v[70:71], v[78:79]
	v_pk_mul_f32 v[72:73], v[72:73], v[80:81]
	v_pk_mul_f32 v[66:67], v[66:67], v[74:75]
	v_pk_mul_f32 v[68:69], v[68:69], v[76:77]
	v_pk_mul_f32 v[78:79], v[78:79], v[248:249] op_sel_hi:[1,0]
	v_pk_mul_f32 v[80:81], v[80:81], v[248:249] op_sel_hi:[1,0]
	v_pk_mul_f32 v[74:75], v[74:75], v[248:249] op_sel_hi:[1,0]
	v_pk_mul_f32 v[76:77], v[76:77], v[248:249] op_sel_hi:[1,0]
	v_exp_f32_e32 v78, v78
	v_exp_f32_e32 v79, v79
	v_exp_f32_e32 v80, v80
	v_exp_f32_e32 v81, v81
	v_exp_f32_e32 v74, v74
	v_exp_f32_e32 v75, v75
	v_exp_f32_e32 v76, v76
	v_exp_f32_e32 v77, v77
	v_pk_fma_f32 v[78:79], v[78:79], v[250:251], v[250:251] op_sel_hi:[1,0,0]
	v_pk_fma_f32 v[80:81], v[80:81], v[250:251], v[250:251] op_sel_hi:[1,0,0]
	v_pk_fma_f32 v[74:75], v[74:75], v[250:251], v[250:251] op_sel_hi:[1,0,0]
	v_pk_fma_f32 v[76:77], v[76:77], v[250:251], v[250:251] op_sel_hi:[1,0,0]
	v_rcp_f32_e32 v78, v78
	v_rcp_f32_e32 v79, v79
	v_rcp_f32_e32 v80, v80
	v_rcp_f32_e32 v81, v81
	v_rcp_f32_e32 v74, v74
	v_rcp_f32_e32 v75, v75
	v_rcp_f32_e32 v76, v76
	v_rcp_f32_e32 v77, v77
	v_pk_mul_f32 v[70:71], v[70:71], v[78:79]
	v_pk_mul_f32 v[72:73], v[72:73], v[80:81]
	v_pk_mul_f32 v[66:67], v[66:67], v[74:75]
	v_pk_mul_f32 v[68:69], v[68:69], v[76:77]
	s_waitcnt lgkmcnt(0)
	global_store_dwordx4 v[140:141], v[90:93], off nt
	v_cvt_pk_bf16_f32 v78, v70, v71
	v_cvt_pk_bf16_f32 v79, v72, v73
	v_cvt_pk_bf16_f32 v80, v66, v67
	v_cvt_pk_bf16_f32 v81, v68, v69
	ds_bpermute_b32 v74, v156, v78
	ds_bpermute_b32 v75, v156, v79
	ds_bpermute_b32 v76, v156, v80
	ds_bpermute_b32 v77, v156, v81
	v_add_co_u32_e32 v142, vcc, 0x54000, v170
	v_addc_co_u32_e32 v143, vcc, 0, v171, vcc
	v_mul_f32_e32 v248, 0xbfb8aa3b, v243
	v_mul_f32_e32 v250, v243, v243
	v_rcp_f32_e32 v250, v250
	v_pk_mul_f32 v[50:51], v[50:51], v[62:63]
	v_pk_mul_f32 v[52:53], v[52:53], v[64:65]
	v_pk_mul_f32 v[42:43], v[42:43], v[58:59]
	v_pk_mul_f32 v[44:45], v[44:45], v[60:61]
	v_pk_mul_f32 v[62:63], v[62:63], v[248:249] op_sel_hi:[1,0]
	v_pk_mul_f32 v[64:65], v[64:65], v[248:249] op_sel_hi:[1,0]
	v_pk_mul_f32 v[58:59], v[58:59], v[248:249] op_sel_hi:[1,0]
	v_pk_mul_f32 v[60:61], v[60:61], v[248:249] op_sel_hi:[1,0]
	v_exp_f32_e32 v62, v62
	v_exp_f32_e32 v63, v63
	v_exp_f32_e32 v64, v64
	v_exp_f32_e32 v65, v65
	v_exp_f32_e32 v58, v58
	v_exp_f32_e32 v59, v59
	v_exp_f32_e32 v60, v60
	v_exp_f32_e32 v61, v61
	v_pk_fma_f32 v[62:63], v[62:63], v[250:251], v[250:251] op_sel_hi:[1,0,0]
	v_pk_fma_f32 v[64:65], v[64:65], v[250:251], v[250:251] op_sel_hi:[1,0,0]
	v_pk_fma_f32 v[58:59], v[58:59], v[250:251], v[250:251] op_sel_hi:[1,0,0]
	v_pk_fma_f32 v[60:61], v[60:61], v[250:251], v[250:251] op_sel_hi:[1,0,0]
	v_rcp_f32_e32 v62, v62
	v_rcp_f32_e32 v63, v63
	v_rcp_f32_e32 v64, v64
	v_rcp_f32_e32 v65, v65
	v_rcp_f32_e32 v58, v58
	v_rcp_f32_e32 v59, v59
	v_rcp_f32_e32 v60, v60
	v_rcp_f32_e32 v61, v61
	v_pk_mul_f32 v[50:51], v[50:51], v[62:63]
	v_pk_mul_f32 v[52:53], v[52:53], v[64:65]
	v_pk_mul_f32 v[42:43], v[42:43], v[58:59]
	v_pk_mul_f32 v[44:45], v[44:45], v[60:61]
	s_waitcnt lgkmcnt(0)
	global_store_dwordx4 v[142:143], v[74:77], off nt
	v_cvt_pk_bf16_f32 v62, v50, v51
	v_cvt_pk_bf16_f32 v63, v52, v53
	v_cvt_pk_bf16_f32 v64, v42, v43
	v_cvt_pk_bf16_f32 v65, v44, v45
	ds_bpermute_b32 v58, v156, v62
	ds_bpermute_b32 v59, v156, v63
	ds_bpermute_b32 v60, v156, v64
	ds_bpermute_b32 v61, v156, v65
	v_add_co_u32_e32 v140, vcc, 0xe0000, v170
	v_addc_co_u32_e32 v141, vcc, 0, v171, vcc
	v_mul_f32_e32 v248, 0xbfb8aa3b, v242
	v_mul_f32_e32 v250, v242, v242
	v_rcp_f32_e32 v250, v250
	v_pk_mul_f32 v[54:55], v[54:55], v[38:39]
	v_pk_mul_f32 v[56:57], v[56:57], v[40:41]
	v_pk_mul_f32 v[46:47], v[46:47], v[34:35]
	v_pk_mul_f32 v[48:49], v[48:49], v[36:37]
	v_pk_mul_f32 v[38:39], v[38:39], v[248:249] op_sel_hi:[1,0]
	v_pk_mul_f32 v[40:41], v[40:41], v[248:249] op_sel_hi:[1,0]
	v_pk_mul_f32 v[34:35], v[34:35], v[248:249] op_sel_hi:[1,0]
	v_pk_mul_f32 v[36:37], v[36:37], v[248:249] op_sel_hi:[1,0]
	v_exp_f32_e32 v38, v38
	v_exp_f32_e32 v39, v39
	v_exp_f32_e32 v40, v40
	v_exp_f32_e32 v41, v41
	v_exp_f32_e32 v34, v34
	v_exp_f32_e32 v35, v35
	v_exp_f32_e32 v36, v36
	v_exp_f32_e32 v37, v37
	v_pk_fma_f32 v[38:39], v[38:39], v[250:251], v[250:251] op_sel_hi:[1,0,0]
	v_pk_fma_f32 v[40:41], v[40:41], v[250:251], v[250:251] op_sel_hi:[1,0,0]
	v_pk_fma_f32 v[34:35], v[34:35], v[250:251], v[250:251] op_sel_hi:[1,0,0]
	v_pk_fma_f32 v[36:37], v[36:37], v[250:251], v[250:251] op_sel_hi:[1,0,0]
	v_rcp_f32_e32 v38, v38
	v_rcp_f32_e32 v39, v39
	v_rcp_f32_e32 v40, v40
	v_rcp_f32_e32 v41, v41
	v_rcp_f32_e32 v34, v34
	v_rcp_f32_e32 v35, v35
	v_rcp_f32_e32 v36, v36
	v_rcp_f32_e32 v37, v37
	v_pk_mul_f32 v[54:55], v[54:55], v[38:39]
	v_pk_mul_f32 v[56:57], v[56:57], v[40:41]
	v_pk_mul_f32 v[46:47], v[46:47], v[34:35]
	v_pk_mul_f32 v[48:49], v[48:49], v[36:37]
	s_waitcnt lgkmcnt(0)
; __device__ __forceinline__ unsigned cvt_pk_bf16(float lo, float hi) { const f32x2c_t v = {lo, hi}; return __builtin_bit_cast(unsigned, __builtin_convertvector(v, bf16x2c_t)); }
; __device__ __forceinline__ float silu_f(float a) { return a * __builtin_amdgcn_rcpf(1.0f + __builtin_amdgcn_exp2f(a * -1.4426950408889634f)); }
; #define PG8_BAR __builtin_amdgcn_s_barrier()
;     __device__ __forceinline__ void operator()(const f32x4 (&acc)[2][2][4][2], const Unit& u, int wr, int wc, int fr, int fq) const {
;     ...
;         for (int ai = 0; ai < 2; ++ai) {
; #pragma unroll
;             for (int m = 0; m < 4; ++m) { const int row = row0 + ai * HALF + m * 16; const float rs = rs8[ai][m];
;                 const f32x4 a0 = acc[ai][0][m][0] * rs, a1 = acc[ai][0][m][1] * rs, b0 = acc[ai][1][m][0] * rs, b1 = acc[ai][1][m][1] * rs;
;                 f32x4 g0, g1;
; #pragma unroll
;                 for (int j = 0; j < 4; ++j) { g0[j] = silu_f(a0[j]) * b0[j]; g1[j] = silu_f(a1[j]) * b1[j]; }
;                 u32x4 w; w.x = cvt_pk_bf16(g0[0], g0[1]); w.y = cvt_pk_bf16(g0[2], g0[3]); w.z = cvt_pk_bf16(g1[0], g1[1]); w.w = cvt_pk_bf16(g1[2], g1[3]);
;                 w = lane_perm(w, qs4); u32x4* dst = (u32x4*)(O + (size_t)(rowS + ai * HALF + m * 16) * ldo + colS); (void)row;
;                 if constexpr (MOE) __builtin_nontemporal_store(w, dst); else *dst = w; } }
; template <class Epi, class Sched, bool ALIGN_EPI = false, bool SP2 = false>
; __device__ __forceinline__ void gemm_phase(PG8_LAS unsigned char* lds, const Gemm g, const Sched& S, const Epi& E, const bool skip_epi = false) {
;     ...
;         if constexpr (!Epi::AFTER_DRAIN) { if (!skip_epi) E(acc, cur, wr, wc, fr, fq); S.done(cur); }
;         if (!has_next) break;
; #pragma unroll
;         for (int a = 0; a < 2; ++a)
; #pragma unroll
;             for (int b = 0; b < 2; ++b)
; #pragma unroll
;                 for (int m = 0; m < 4; ++m)
; #pragma unroll
;                     for (int n = 0; n < 2; ++n) acc[a][b][m][n] = (f32x4){0.f, 0.f, 0.f, 0.f};
;         cur = nxt; cA = nA; cB = nB; ++ui;
;         if constexpr (Sched::GATHER) { gA[0][0] = gN[0][0]; gA[0][1] = gN[0][1]; gA[1][0] = gN[1][0]; gA[1][1] = gN[1][1]; }
;         if constexpr (ALIGN_EPI) { if (wr == 1) PG8_BAR; }
	global_store_dwordx4 v[140:141], v[58:61], off nt
	v_cvt_pk_bf16_f32 v38, v54, v55
	v_cvt_pk_bf16_f32 v39, v56, v57
	v_cvt_pk_bf16_f32 v40, v46, v47
	v_cvt_pk_bf16_f32 v41, v48, v49
	ds_bpermute_b32 v34, v156, v38
	ds_bpermute_b32 v35, v156, v39
	ds_bpermute_b32 v36, v156, v40
	ds_bpermute_b32 v37, v156, v41
	v_add_co_u32_e32 v142, vcc, 0xfc000, v170
	v_addc_co_u32_e32 v143, vcc, 0, v171, vcc
	v_mul_f32_e32 v248, 0xbfb8aa3b, v241
	v_mul_f32_e32 v250, v241, v241
	v_rcp_f32_e32 v250, v250
	v_pk_mul_f32 v[30:31], v[30:31], v[22:23]
	v_pk_mul_f32 v[32:33], v[32:33], v[24:25]
	v_pk_mul_f32 v[26:27], v[26:27], v[18:19]
	v_pk_mul_f32 v[28:29], v[28:29], v[20:21]
	v_pk_mul_f32 v[22:23], v[22:23], v[248:249] op_sel_hi:[1,0]
	v_pk_mul_f32 v[24:25], v[24:25], v[248:249] op_sel_hi:[1,0]
	v_pk_mul_f32 v[18:19], v[18:19], v[248:249] op_sel_hi:[1,0]
	v_pk_mul_f32 v[20:21], v[20:21], v[248:249] op_sel_hi:[1,0]
	v_exp_f32_e32 v22, v22
	v_exp_f32_e32 v23, v23
	v_exp_f32_e32 v24, v24
	v_exp_f32_e32 v25, v25
	v_exp_f32_e32 v18, v18
	v_exp_f32_e32 v19, v19
	v_exp_f32_e32 v20, v20
	v_exp_f32_e32 v21, v21
	v_pk_fma_f32 v[22:23], v[22:23], v[250:251], v[250:251] op_sel_hi:[1,0,0]
	v_pk_fma_f32 v[24:25], v[24:25], v[250:251], v[250:251] op_sel_hi:[1,0,0]
	v_pk_fma_f32 v[18:19], v[18:19], v[250:251], v[250:251] op_sel_hi:[1,0,0]
	v_pk_fma_f32 v[20:21], v[20:21], v[250:251], v[250:251] op_sel_hi:[1,0,0]
	v_rcp_f32_e32 v22, v22
	v_rcp_f32_e32 v23, v23
	v_rcp_f32_e32 v24, v24
	v_rcp_f32_e32 v25, v25
	v_rcp_f32_e32 v18, v18
	v_rcp_f32_e32 v19, v19
	v_rcp_f32_e32 v20, v20
	v_rcp_f32_e32 v21, v21
	v_pk_mul_f32 v[30:31], v[30:31], v[22:23]
	v_pk_mul_f32 v[32:33], v[32:33], v[24:25]
	v_pk_mul_f32 v[26:27], v[26:27], v[18:19]
	v_pk_mul_f32 v[28:29], v[28:29], v[20:21]
	s_waitcnt lgkmcnt(0)
	global_store_dwordx4 v[142:143], v[34:37], off nt
	v_cvt_pk_bf16_f32 v22, v30, v31
	v_cvt_pk_bf16_f32 v23, v32, v33
	v_cvt_pk_bf16_f32 v24, v26, v27
	v_cvt_pk_bf16_f32 v25, v28, v29
	ds_bpermute_b32 v18, v156, v22
	ds_bpermute_b32 v19, v156, v23
	ds_bpermute_b32 v20, v156, v24
	ds_bpermute_b32 v21, v156, v25
	v_add_co_u32_e32 v140, vcc, 0x118000, v170
	v_addc_co_u32_e32 v141, vcc, 0, v171, vcc
	v_mul_f32_e32 v248, 0xbfb8aa3b, v240
	v_mul_f32_e32 v250, v240, v240
	v_rcp_f32_e32 v250, v250
	v_pk_mul_f32 v[14:15], v[14:15], v[6:7]
	v_pk_mul_f32 v[16:17], v[16:17], v[8:9]
	v_pk_mul_f32 v[10:11], v[10:11], v[2:3]
	v_pk_mul_f32 v[12:13], v[12:13], v[4:5]
	v_pk_mul_f32 v[6:7], v[6:7], v[248:249] op_sel_hi:[1,0]
	v_pk_mul_f32 v[8:9], v[8:9], v[248:249] op_sel_hi:[1,0]
	v_pk_mul_f32 v[2:3], v[2:3], v[248:249] op_sel_hi:[1,0]
	v_pk_mul_f32 v[4:5], v[4:5], v[248:249] op_sel_hi:[1,0]
	v_exp_f32_e32 v6, v6
	v_exp_f32_e32 v7, v7
	v_exp_f32_e32 v8, v8
	v_exp_f32_e32 v9, v9
	v_exp_f32_e32 v2, v2
	v_exp_f32_e32 v3, v3
	v_exp_f32_e32 v4, v4
	v_exp_f32_e32 v5, v5
	v_pk_fma_f32 v[6:7], v[6:7], v[250:251], v[250:251] op_sel_hi:[1,0,0]
	v_pk_fma_f32 v[8:9], v[8:9], v[250:251], v[250:251] op_sel_hi:[1,0,0]
	v_pk_fma_f32 v[2:3], v[2:3], v[250:251], v[250:251] op_sel_hi:[1,0,0]
	v_pk_fma_f32 v[4:5], v[4:5], v[250:251], v[250:251] op_sel_hi:[1,0,0]
	v_rcp_f32_e32 v6, v6
	v_rcp_f32_e32 v7, v7
	v_rcp_f32_e32 v8, v8
	v_rcp_f32_e32 v9, v9
	v_rcp_f32_e32 v2, v2
	v_rcp_f32_e32 v3, v3
	v_rcp_f32_e32 v4, v4
	v_rcp_f32_e32 v5, v5
	v_pk_mul_f32 v[14:15], v[14:15], v[6:7]
	v_pk_mul_f32 v[16:17], v[16:17], v[8:9]
	v_pk_mul_f32 v[10:11], v[10:11], v[2:3]
	v_pk_mul_f32 v[12:13], v[12:13], v[4:5]
	s_waitcnt lgkmcnt(0)
	global_store_dwordx4 v[140:141], v[18:21], off nt
	v_cvt_pk_bf16_f32 v6, v14, v15
	v_cvt_pk_bf16_f32 v7, v16, v17
	v_cvt_pk_bf16_f32 v8, v10, v11
	v_cvt_pk_bf16_f32 v9, v12, v13
	ds_bpermute_b32 v2, v156, v6
	ds_bpermute_b32 v3, v156, v7
	ds_bpermute_b32 v4, v156, v8
	ds_bpermute_b32 v5, v156, v9
	v_add_co_u32_e32 v142, vcc, 0x134000, v170
	v_addc_co_u32_e32 v143, vcc, 0, v171, vcc
	s_waitcnt lgkmcnt(0)
	global_store_dwordx4 v[142:143], v[2:5], off nt
	s_setprio 0
	s_and_b64 vcc, exec, s[4:5]
	s_mov_b64 s[4:5], -1
	s_cbranch_vccnz .LBB0_1718
	s_andn2_b64 vcc, exec, s[10:11]
	s_cbranch_vccnz .LBB0_1717
	s_barrier
	s_branch .LBB0_1717
